# v64 + layer-0 conversion loop gain loads batched + LoRA decay prefix via v_add_f32_dpp (2 instr per pair per stage instead of 3)
# baseline (speedup 1.0000x reference)
.LBB0_22:
	s_andn2_b64 vcc, exec, s[26:27]
	s_cbranch_vccnz .LBB0_32
	s_mov_b64 s[8:9], s[58:59]
	s_load_dwordx2 s[30:31], s[8:9], 0x38
	s_add_i32 s26, s33, 0xec80
	s_lshl_b64 s[8:9], s[20:21], 2
	v_mov_b32_e32 v64, 1.0
	v_mov_b32_e32 v66, 1.0
	s_waitcnt lgkmcnt(0)
	s_add_u32 s36, s30, s8
	s_addc_u32 s37, s31, s9
	s_lshr_b32 s9, s26, 1
	s_and_b32 s9, s9, 0x7fc0
	s_and_b32 s8, s0, 0xfe0
	v_add_u32_e32 v62, s9, v33
	s_lshl_b32 s92, s8, 2
	v_ashrrev_i32_e32 v63, 31, v62
	v_lshl_add_u64 v[0:1], v[38:39], 0, s[92:93]
	v_lshlrev_b64 v[2:3], 14, v[62:63]
	v_lshl_add_u64 v[0:1], v[0:1], 0, v[2:3]
	s_mov_b32 s26, 0x20000
	v_add_co_u32_e32 v2, vcc, s26, v0
	s_mov_b32 s26, 0x40000
	s_nop 0
	v_addc_co_u32_e32 v3, vcc, 0, v1, vcc
	global_load_dwordx4 v[28:31], v[0:1], off nt
	global_load_dwordx4 v[24:27], v[2:3], off nt
	v_add_co_u32_e32 v2, vcc, s26, v0
	s_mov_b32 s26, 0x60000
	s_nop 0
	v_addc_co_u32_e32 v3, vcc, 0, v1, vcc
	v_add_co_u32_e32 v4, vcc, s26, v0
	s_mov_b32 s26, 0x80000
	s_nop 0
	v_addc_co_u32_e32 v5, vcc, 0, v1, vcc
	global_load_dwordx4 v[20:23], v[2:3], off nt
	global_load_dwordx4 v[16:19], v[4:5], off nt
	v_add_co_u32_e32 v2, vcc, s26, v0
	s_mov_b32 s26, 0xa0000
	s_nop 0
	v_addc_co_u32_e32 v3, vcc, 0, v1, vcc
	v_add_co_u32_e32 v4, vcc, s26, v0
	s_cmp_lg_u64 s[30:31], 0
	s_nop 0
	v_addc_co_u32_e32 v5, vcc, 0, v1, vcc
	global_load_dwordx4 v[12:15], v[2:3], off nt
	global_load_dwordx4 v[8:11], v[4:5], off nt
	v_add_co_u32_e32 v2, vcc, 0xc0000, v0
	s_cselect_b64 s[26:27], -1, 0
	s_nop 0
	v_addc_co_u32_e32 v3, vcc, 0, v1, vcc
	v_add_co_u32_e32 v0, vcc, 0xe0000, v0
	s_cmp_eq_u64 s[30:31], 0
	s_nop 0
	v_addc_co_u32_e32 v1, vcc, 0, v1, vcc
	global_load_dwordx4 v[4:7], v[2:3], off nt
	s_nop 0
	global_load_dwordx4 v[0:3], v[0:1], off nt
	v_lshl_add_u64 v[62:63], v[62:63], 2, s[36:37]
	s_cbranch_scc1 .LBB0_25
	global_load_dword v100, v[62:63], off
	global_load_dword v101, v[62:63], off offset:32
	global_load_dword v102, v[62:63], off offset:64
	global_load_dword v103, v[62:63], off offset:96
	global_load_dword v104, v[62:63], off offset:128
	global_load_dword v105, v[62:63], off offset:160
	global_load_dword v106, v[62:63], off offset:192
	global_load_dword v107, v[62:63], off offset:224
	s_waitcnt vmcnt(0)
	v_mov_b32_e32 v88, v100
	v_mov_b32_e32 v66, v101
	v_pk_mul_f32 v[28:29], v[28:29], v[88:89] op_sel_hi:[1,0]
	v_pk_mul_f32 v[30:31], v[30:31], v[88:89] op_sel_hi:[1,0]
.LBB0_25:
	s_waitcnt vmcnt(0)
	v_pk_mul_f32 v[24:25], v[24:25], v[66:67] op_sel_hi:[1,0]
	ds_write2_b32 v72, v28, v29 offset1:1
	ds_write2_b32 v72, v30, v31 offset0:2 offset1:3
	ds_write2_b32 v73, v24, v25 offset1:1
	v_pk_mul_f32 v[24:25], v[26:27], v[66:67] op_sel_hi:[1,0]
	v_cndmask_b32_e64 v26, 0, 1, s[26:27]
	v_cmp_ne_u32_e64 s[36:37], 1, v26
	s_andn2_b64 vcc, exec, s[26:27]
	ds_write2_b32 v74, v24, v25 offset1:1
	s_cbranch_vccnz .LBB0_27
	v_mov_b32_e32 v24, v102
	v_mov_b32_e32 v64, v103
	s_waitcnt vmcnt(1)
	v_pk_mul_f32 v[20:21], v[20:21], v[24:25] op_sel_hi:[1,0]
	v_pk_mul_f32 v[22:23], v[22:23], v[24:25] op_sel_hi:[1,0]
.LBB0_27:
	s_waitcnt vmcnt(0)
	v_pk_mul_f32 v[16:17], v[16:17], v[64:65] op_sel_hi:[1,0]
	ds_write2_b32 v75, v20, v21 offset1:1
	ds_write2_b32 v76, v22, v23 offset1:1
	ds_write2_b32 v77, v16, v17 offset1:1
	v_pk_mul_f32 v[16:17], v[18:19], v[64:65] op_sel_hi:[1,0]
	ds_write2_b32 v78, v16, v17 offset1:1
	v_mov_b32_e32 v16, 1.0
	s_and_b64 vcc, exec, s[36:37]
	v_mov_b32_e32 v18, 1.0
	s_cbranch_vccnz .LBB0_29
	v_mov_b32_e32 v20, v104
	v_mov_b32_e32 v18, v105
	s_waitcnt vmcnt(1)
	v_pk_mul_f32 v[12:13], v[12:13], v[20:21] op_sel_hi:[1,0]
	v_pk_mul_f32 v[14:15], v[14:15], v[20:21] op_sel_hi:[1,0]
.LBB0_29:
	v_add_u32_e32 v17, v65, v71
	ds_write2_b32 v17, v12, v13 offset1:1
	ds_write2_b32 v17, v14, v15 offset0:2 offset1:3
	s_waitcnt vmcnt(0)
	v_pk_mul_f32 v[8:9], v[8:9], v[18:19] op_sel_hi:[1,0]
	v_add_u32_e32 v12, 0x420, v17
	ds_write2_b32 v12, v8, v9 offset1:1
	v_pk_mul_f32 v[8:9], v[10:11], v[18:19] op_sel_hi:[1,0]
	v_add_u32_e32 v10, 0x428, v17
	s_and_b64 vcc, exec, s[36:37]
	ds_write2_b32 v10, v8, v9 offset1:1
	s_cbranch_vccnz .LBB0_31
	v_mov_b32_e32 v8, v106
	v_mov_b32_e32 v16, v107
	s_waitcnt vmcnt(1)
	v_pk_mul_f32 v[4:5], v[4:5], v[8:9] op_sel_hi:[1,0]
	v_pk_mul_f32 v[6:7], v[6:7], v[8:9] op_sel_hi:[1,0]

.LBB0_45:
	s_andn2_b64 vcc, exec, s[26:27]
	s_cbranch_vccnz .LBB0_15
	s_mov_b64 s[8:9], s[58:59]
	s_load_dwordx2 s[8:9], s[8:9], 0x28
	s_lshl_b64 s[26:27], s[20:21], 2
	s_mul_hi_i32 s30, s33, 0x88888889
	v_mov_b32_e32 v64, 1.0
	v_mov_b32_e32 v66, 1.0
	s_waitcnt lgkmcnt(0)
	s_add_u32 s36, s8, s26
	s_addc_u32 s37, s9, s27
	s_add_i32 s30, s30, s33
	s_lshr_b32 s26, s30, 31
	s_ashr_i32 s27, s30, 6
	s_add_i32 s26, s27, s26
	s_lshl_b32 s30, s26, 6
	s_mulk_i32 s26, 0xf100
	s_add_i32 s26, s0, s26
	v_add_u32_e32 v62, s30, v33
	s_ashr_i32 s27, s26, 31
	v_lshl_add_u64 v[0:1], s[26:27], 2, v[58:59]
	s_movk_i32 s27, 0x3c00
	v_add_u32_e32 v4, 8, v62
	v_mad_i64_i32 v[2:3], s[38:39], v62, s27, v[0:1]
	v_mad_i64_i32 v[4:5], s[38:39], v4, s27, v[0:1]
	global_load_dwordx4 v[28:31], v[2:3], off nt
	global_load_dwordx4 v[24:27], v[4:5], off nt
	v_add_u32_e32 v2, 16, v62
	v_add_u32_e32 v4, 24, v62
	v_mad_i64_i32 v[2:3], s[38:39], v2, s27, v[0:1]
	v_mad_i64_i32 v[4:5], s[38:39], v4, s27, v[0:1]
	global_load_dwordx4 v[20:23], v[2:3], off nt
	global_load_dwordx4 v[16:19], v[4:5], off nt
	v_add_u32_e32 v2, 32, v62
	v_add_u32_e32 v4, 40, v62
	v_mad_i64_i32 v[2:3], s[38:39], v2, s27, v[0:1]
	v_mad_i64_i32 v[4:5], s[38:39], v4, s27, v[0:1]
	global_load_dwordx4 v[12:15], v[2:3], off nt
	global_load_dwordx4 v[8:11], v[4:5], off nt
	v_add_u32_e32 v2, 48, v62
	v_add_u32_e32 v4, 56, v62
	v_mad_i64_i32 v[2:3], s[38:39], v2, s27, v[0:1]
	v_mad_i64_i32 v[0:1], s[38:39], v4, s27, v[0:1]
	global_load_dwordx4 v[4:7], v[2:3], off nt
	s_nop 0
	global_load_dwordx4 v[0:3], v[0:1], off nt
	v_ashrrev_i32_e32 v63, 31, v62
	s_cmp_lg_u64 s[8:9], 0
	s_cselect_b64 s[38:39], -1, 0
	s_cmp_eq_u64 s[8:9], 0
	v_lshl_add_u64 v[62:63], v[62:63], 2, s[36:37]
	s_cbranch_scc1 .LBB0_48
	global_load_dword v100, v[62:63], off
	global_load_dword v101, v[62:63], off offset:32
	global_load_dword v102, v[62:63], off offset:64
	global_load_dword v103, v[62:63], off offset:96
	global_load_dword v104, v[62:63], off offset:128
	global_load_dword v105, v[62:63], off offset:160
	global_load_dword v106, v[62:63], off offset:192
	global_load_dword v107, v[62:63], off offset:224
	s_waitcnt vmcnt(0)
	v_mov_b32_e32 v88, v100
	v_mov_b32_e32 v66, v101
	v_pk_mul_f32 v[28:29], v[28:29], v[88:89] op_sel_hi:[1,0]
	v_pk_mul_f32 v[30:31], v[30:31], v[88:89] op_sel_hi:[1,0]
.LBB0_48:
	s_waitcnt vmcnt(0)
	v_pk_mul_f32 v[24:25], v[24:25], v[66:67] op_sel_hi:[1,0]
	ds_write2_b32 v72, v28, v29 offset1:1
	ds_write2_b32 v72, v30, v31 offset0:2 offset1:3
	ds_write2_b32 v73, v24, v25 offset1:1
	v_pk_mul_f32 v[24:25], v[26:27], v[66:67] op_sel_hi:[1,0]
	v_cndmask_b32_e64 v26, 0, 1, s[38:39]
	v_cmp_ne_u32_e64 s[36:37], 1, v26
	s_andn2_b64 vcc, exec, s[38:39]
	ds_write2_b32 v74, v24, v25 offset1:1
	s_cbranch_vccnz .LBB0_50
	v_mov_b32_e32 v24, v102
	v_mov_b32_e32 v64, v103
	s_waitcnt vmcnt(1)
	v_pk_mul_f32 v[20:21], v[20:21], v[24:25] op_sel_hi:[1,0]
	v_pk_mul_f32 v[22:23], v[22:23], v[24:25] op_sel_hi:[1,0]

.LBB0_52:
	v_add_u32_e32 v17, v65, v71
	ds_write2_b32 v17, v12, v13 offset1:1
	ds_write2_b32 v17, v14, v15 offset0:2 offset1:3
	s_waitcnt vmcnt(0)
	v_pk_mul_f32 v[8:9], v[8:9], v[18:19] op_sel_hi:[1,0]
	v_add_u32_e32 v12, 0x420, v17
	ds_write2_b32 v12, v8, v9 offset1:1
	v_pk_mul_f32 v[8:9], v[10:11], v[18:19] op_sel_hi:[1,0]
	v_add_u32_e32 v10, 0x428, v17
	s_and_b64 vcc, exec, s[36:37]
	ds_write2_b32 v10, v8, v9 offset1:1
	s_cbranch_vccnz .LBB0_14
	v_mov_b32_e32 v8, v106
	v_mov_b32_e32 v16, v107
	s_waitcnt vmcnt(1)
	v_pk_mul_f32 v[4:5], v[4:5], v[8:9] op_sel_hi:[1,0]
	v_pk_mul_f32 v[6:7], v[6:7], v[8:9] op_sel_hi:[1,0]
	s_branch .LBB0_14

.LBB0_724:
	v_pk_mul_f32 v[138:139], v[158:159], s[6:7] op_sel_hi:[1,0]
	s_nop 1
	v_mov_b32_dpp v138, v138 row_shr:1 row_mask:0xf bank_mask:0xf bound_ctrl:1
	v_mov_b32_dpp v139, v139 row_shr:1 row_mask:0xf bank_mask:0xf bound_ctrl:1
	v_pk_fma_f32 v[138:139], v[158:159], s[6:7], v[138:139] op_sel_hi:[1,0,1]
	s_nop 1
	v_add_f32_dpp v138, v138, v138 row_shr:2 row_mask:0xf bank_mask:0xf bound_ctrl:1
	v_add_f32_dpp v139, v139, v139 row_shr:2 row_mask:0xf bank_mask:0xf bound_ctrl:1
	s_nop 1
	v_add_f32_dpp v138, v138, v138 row_shr:4 row_mask:0xf bank_mask:0xf bound_ctrl:1
	v_add_f32_dpp v139, v139, v139 row_shr:4 row_mask:0xf bank_mask:0xf bound_ctrl:1
	s_nop 1
	v_add_f32_dpp v138, v138, v138 row_shr:8 row_mask:0xf bank_mask:0xf bound_ctrl:1
	v_add_f32_dpp v139, v139, v139 row_shr:8 row_mask:0xf bank_mask:0xf bound_ctrl:1
	v_pk_mul_f32 v[140:141], v[156:157], s[6:7] op_sel_hi:[1,0]
	v_cvt_pk_f16_f32 v138, v138, v139
	s_nop 0
	v_mov_b32_dpp v140, v140 row_shr:1 row_mask:0xf bank_mask:0xf bound_ctrl:1
	v_mov_b32_dpp v141, v141 row_shr:1 row_mask:0xf bank_mask:0xf bound_ctrl:1
	v_pk_fma_f32 v[140:141], v[156:157], s[6:7], v[140:141] op_sel_hi:[1,0,1]
	s_nop 1
	v_add_f32_dpp v140, v140, v140 row_shr:2 row_mask:0xf bank_mask:0xf bound_ctrl:1
	v_add_f32_dpp v141, v141, v141 row_shr:2 row_mask:0xf bank_mask:0xf bound_ctrl:1
	s_nop 1
	v_add_f32_dpp v140, v140, v140 row_shr:4 row_mask:0xf bank_mask:0xf bound_ctrl:1
	v_add_f32_dpp v141, v141, v141 row_shr:4 row_mask:0xf bank_mask:0xf bound_ctrl:1
	s_nop 1
	v_add_f32_dpp v140, v140, v140 row_shr:8 row_mask:0xf bank_mask:0xf bound_ctrl:1
	v_add_f32_dpp v141, v141, v141 row_shr:8 row_mask:0xf bank_mask:0xf bound_ctrl:1
	v_pk_mul_f32 v[156:157], v[144:145], s[6:7] op_sel_hi:[1,0]
	v_cvt_pk_f16_f32 v140, v140, v141
	s_nop 0
	v_mov_b32_dpp v156, v156 row_shr:1 row_mask:0xf bank_mask:0xf bound_ctrl:1
	v_mov_b32_dpp v157, v157 row_shr:1 row_mask:0xf bank_mask:0xf bound_ctrl:1
	v_pk_fma_f32 v[144:145], v[144:145], s[6:7], v[156:157] op_sel_hi:[1,0,1]
	s_nop 1
	v_add_f32_dpp v144, v144, v144 row_shr:2 row_mask:0xf bank_mask:0xf bound_ctrl:1
	v_add_f32_dpp v145, v145, v145 row_shr:2 row_mask:0xf bank_mask:0xf bound_ctrl:1
	s_nop 1
	v_add_f32_dpp v144, v144, v144 row_shr:4 row_mask:0xf bank_mask:0xf bound_ctrl:1
	v_add_f32_dpp v145, v145, v145 row_shr:4 row_mask:0xf bank_mask:0xf bound_ctrl:1
	s_nop 1
	v_add_f32_dpp v144, v144, v144 row_shr:8 row_mask:0xf bank_mask:0xf bound_ctrl:1
	v_add_f32_dpp v145, v145, v145 row_shr:8 row_mask:0xf bank_mask:0xf bound_ctrl:1
	v_pk_mul_f32 v[156:157], v[142:143], s[6:7] op_sel_hi:[1,0]
	v_cvt_pk_f16_f32 v139, v144, v145
	s_nop 0
	v_mov_b32_dpp v156, v156 row_shr:1 row_mask:0xf bank_mask:0xf bound_ctrl:1
	v_mov_b32_dpp v157, v157 row_shr:1 row_mask:0xf bank_mask:0xf bound_ctrl:1
	v_pk_fma_f32 v[142:143], v[142:143], s[6:7], v[156:157] op_sel_hi:[1,0,1]
	s_nop 1
	v_add_f32_dpp v142, v142, v142 row_shr:2 row_mask:0xf bank_mask:0xf bound_ctrl:1
	v_add_f32_dpp v143, v143, v143 row_shr:2 row_mask:0xf bank_mask:0xf bound_ctrl:1
	s_nop 1
	v_add_f32_dpp v142, v142, v142 row_shr:4 row_mask:0xf bank_mask:0xf bound_ctrl:1
	v_add_f32_dpp v143, v143, v143 row_shr:4 row_mask:0xf bank_mask:0xf bound_ctrl:1
	s_nop 1
	v_add_f32_dpp v142, v142, v142 row_shr:8 row_mask:0xf bank_mask:0xf bound_ctrl:1
	v_add_f32_dpp v143, v143, v143 row_shr:8 row_mask:0xf bank_mask:0xf bound_ctrl:1
	s_nop 0
	v_cvt_pk_f16_f32 v141, v142, v143

.LBB0_729:
	s_andn2_b64 vcc, exec, s[22:23]
	s_cbranch_vccnz .LBB0_731
	v_pk_mul_f32 v[130:131], v[140:141], s[6:7] op_sel_hi:[1,0]
	s_nop 1
	v_mov_b32_dpp v130, v130 row_shr:1 row_mask:0xf bank_mask:0xf bound_ctrl:1
	v_mov_b32_dpp v131, v131 row_shr:1 row_mask:0xf bank_mask:0xf bound_ctrl:1
	v_pk_fma_f32 v[130:131], v[140:141], s[6:7], v[130:131] op_sel_hi:[1,0,1]
	s_nop 1
	v_add_f32_dpp v130, v130, v130 row_shr:2 row_mask:0xf bank_mask:0xf bound_ctrl:1
	v_add_f32_dpp v131, v131, v131 row_shr:2 row_mask:0xf bank_mask:0xf bound_ctrl:1
	s_nop 1
	v_add_f32_dpp v130, v130, v130 row_shr:4 row_mask:0xf bank_mask:0xf bound_ctrl:1
	v_add_f32_dpp v131, v131, v131 row_shr:4 row_mask:0xf bank_mask:0xf bound_ctrl:1
	s_nop 1
	v_add_f32_dpp v130, v130, v130 row_shr:8 row_mask:0xf bank_mask:0xf bound_ctrl:1
	v_add_f32_dpp v131, v131, v131 row_shr:8 row_mask:0xf bank_mask:0xf bound_ctrl:1
	v_pk_mul_f32 v[132:133], v[138:139], s[6:7] op_sel_hi:[1,0]
	v_cvt_pk_f16_f32 v130, v130, v131
	s_nop 0
	v_mov_b32_dpp v132, v132 row_shr:1 row_mask:0xf bank_mask:0xf bound_ctrl:1
	v_mov_b32_dpp v133, v133 row_shr:1 row_mask:0xf bank_mask:0xf bound_ctrl:1
	v_pk_fma_f32 v[132:133], v[138:139], s[6:7], v[132:133] op_sel_hi:[1,0,1]
	s_nop 1
	v_add_f32_dpp v132, v132, v132 row_shr:2 row_mask:0xf bank_mask:0xf bound_ctrl:1
	v_add_f32_dpp v133, v133, v133 row_shr:2 row_mask:0xf bank_mask:0xf bound_ctrl:1
	s_nop 1
	v_add_f32_dpp v132, v132, v132 row_shr:4 row_mask:0xf bank_mask:0xf bound_ctrl:1
	v_add_f32_dpp v133, v133, v133 row_shr:4 row_mask:0xf bank_mask:0xf bound_ctrl:1
	s_nop 1
	v_add_f32_dpp v132, v132, v132 row_shr:8 row_mask:0xf bank_mask:0xf bound_ctrl:1
	v_add_f32_dpp v133, v133, v133 row_shr:8 row_mask:0xf bank_mask:0xf bound_ctrl:1
	v_pk_mul_f32 v[138:139], v[136:137], s[6:7] op_sel_hi:[1,0]
	v_cvt_pk_f16_f32 v132, v132, v133
	s_nop 0
	v_mov_b32_dpp v138, v138 row_shr:1 row_mask:0xf bank_mask:0xf bound_ctrl:1
	v_mov_b32_dpp v139, v139 row_shr:1 row_mask:0xf bank_mask:0xf bound_ctrl:1
	v_pk_fma_f32 v[136:137], v[136:137], s[6:7], v[138:139] op_sel_hi:[1,0,1]
	s_nop 1
	v_add_f32_dpp v136, v136, v136 row_shr:2 row_mask:0xf bank_mask:0xf bound_ctrl:1
	v_add_f32_dpp v137, v137, v137 row_shr:2 row_mask:0xf bank_mask:0xf bound_ctrl:1
	s_nop 1
	v_add_f32_dpp v136, v136, v136 row_shr:4 row_mask:0xf bank_mask:0xf bound_ctrl:1
	v_add_f32_dpp v137, v137, v137 row_shr:4 row_mask:0xf bank_mask:0xf bound_ctrl:1
	s_nop 1
	v_add_f32_dpp v136, v136, v136 row_shr:8 row_mask:0xf bank_mask:0xf bound_ctrl:1
	v_add_f32_dpp v137, v137, v137 row_shr:8 row_mask:0xf bank_mask:0xf bound_ctrl:1
	v_pk_mul_f32 v[138:139], v[134:135], s[6:7] op_sel_hi:[1,0]
	v_cvt_pk_f16_f32 v131, v136, v137
	s_nop 0
	v_mov_b32_dpp v138, v138 row_shr:1 row_mask:0xf bank_mask:0xf bound_ctrl:1
	v_mov_b32_dpp v139, v139 row_shr:1 row_mask:0xf bank_mask:0xf bound_ctrl:1
	v_pk_fma_f32 v[134:135], v[134:135], s[6:7], v[138:139] op_sel_hi:[1,0,1]
	s_nop 1
	v_add_f32_dpp v134, v134, v134 row_shr:2 row_mask:0xf bank_mask:0xf bound_ctrl:1
	v_add_f32_dpp v135, v135, v135 row_shr:2 row_mask:0xf bank_mask:0xf bound_ctrl:1
	s_nop 1
	v_add_f32_dpp v134, v134, v134 row_shr:4 row_mask:0xf bank_mask:0xf bound_ctrl:1
	v_add_f32_dpp v135, v135, v135 row_shr:4 row_mask:0xf bank_mask:0xf bound_ctrl:1
	s_nop 1
	v_add_f32_dpp v134, v134, v134 row_shr:8 row_mask:0xf bank_mask:0xf bound_ctrl:1
	v_add_f32_dpp v135, v135, v135 row_shr:8 row_mask:0xf bank_mask:0xf bound_ctrl:1
	s_nop 0
	v_cvt_pk_f16_f32 v133, v134, v135

.LBB0_734:
	v_pk_mul_f32 v[120:121], v[132:133], s[6:7] op_sel_hi:[1,0]
	s_nop 1
	v_mov_b32_dpp v120, v120 row_shr:1 row_mask:0xf bank_mask:0xf bound_ctrl:1
	v_mov_b32_dpp v121, v121 row_shr:1 row_mask:0xf bank_mask:0xf bound_ctrl:1
	v_pk_fma_f32 v[120:121], v[132:133], s[6:7], v[120:121] op_sel_hi:[1,0,1]
	s_nop 1
	v_add_f32_dpp v120, v120, v120 row_shr:2 row_mask:0xf bank_mask:0xf bound_ctrl:1
	v_add_f32_dpp v121, v121, v121 row_shr:2 row_mask:0xf bank_mask:0xf bound_ctrl:1
	s_nop 1
	v_add_f32_dpp v120, v120, v120 row_shr:4 row_mask:0xf bank_mask:0xf bound_ctrl:1
	v_add_f32_dpp v121, v121, v121 row_shr:4 row_mask:0xf bank_mask:0xf bound_ctrl:1
	s_nop 1
	v_add_f32_dpp v120, v120, v120 row_shr:8 row_mask:0xf bank_mask:0xf bound_ctrl:1
	v_add_f32_dpp v121, v121, v121 row_shr:8 row_mask:0xf bank_mask:0xf bound_ctrl:1
	v_pk_mul_f32 v[122:123], v[130:131], s[6:7] op_sel_hi:[1,0]
	v_cvt_pk_f16_f32 v120, v120, v121
	s_nop 0
	v_mov_b32_dpp v122, v122 row_shr:1 row_mask:0xf bank_mask:0xf bound_ctrl:1
	v_mov_b32_dpp v123, v123 row_shr:1 row_mask:0xf bank_mask:0xf bound_ctrl:1
	v_pk_fma_f32 v[122:123], v[130:131], s[6:7], v[122:123] op_sel_hi:[1,0,1]
	s_nop 1
	v_add_f32_dpp v122, v122, v122 row_shr:2 row_mask:0xf bank_mask:0xf bound_ctrl:1
	v_add_f32_dpp v123, v123, v123 row_shr:2 row_mask:0xf bank_mask:0xf bound_ctrl:1
	s_nop 1
	v_add_f32_dpp v122, v122, v122 row_shr:4 row_mask:0xf bank_mask:0xf bound_ctrl:1
	v_add_f32_dpp v123, v123, v123 row_shr:4 row_mask:0xf bank_mask:0xf bound_ctrl:1
	s_nop 1
	v_add_f32_dpp v122, v122, v122 row_shr:8 row_mask:0xf bank_mask:0xf bound_ctrl:1
	v_add_f32_dpp v123, v123, v123 row_shr:8 row_mask:0xf bank_mask:0xf bound_ctrl:1
	v_pk_mul_f32 v[130:131], v[126:127], s[6:7] op_sel_hi:[1,0]
	v_cvt_pk_f16_f32 v122, v122, v123
	s_nop 0
	v_mov_b32_dpp v130, v130 row_shr:1 row_mask:0xf bank_mask:0xf bound_ctrl:1
	v_mov_b32_dpp v131, v131 row_shr:1 row_mask:0xf bank_mask:0xf bound_ctrl:1
	v_pk_fma_f32 v[126:127], v[126:127], s[6:7], v[130:131] op_sel_hi:[1,0,1]
	s_nop 1
	v_add_f32_dpp v126, v126, v126 row_shr:2 row_mask:0xf bank_mask:0xf bound_ctrl:1
	v_add_f32_dpp v127, v127, v127 row_shr:2 row_mask:0xf bank_mask:0xf bound_ctrl:1
	s_nop 1
	v_add_f32_dpp v126, v126, v126 row_shr:4 row_mask:0xf bank_mask:0xf bound_ctrl:1
	v_add_f32_dpp v127, v127, v127 row_shr:4 row_mask:0xf bank_mask:0xf bound_ctrl:1
	s_nop 1
	v_add_f32_dpp v126, v126, v126 row_shr:8 row_mask:0xf bank_mask:0xf bound_ctrl:1
	v_add_f32_dpp v127, v127, v127 row_shr:8 row_mask:0xf bank_mask:0xf bound_ctrl:1
	v_pk_mul_f32 v[130:131], v[124:125], s[6:7] op_sel_hi:[1,0]
	v_cvt_pk_f16_f32 v121, v126, v127
	s_nop 0
	v_mov_b32_dpp v130, v130 row_shr:1 row_mask:0xf bank_mask:0xf bound_ctrl:1
	v_mov_b32_dpp v131, v131 row_shr:1 row_mask:0xf bank_mask:0xf bound_ctrl:1
	v_pk_fma_f32 v[124:125], v[124:125], s[6:7], v[130:131] op_sel_hi:[1,0,1]
	s_nop 1
	v_add_f32_dpp v124, v124, v124 row_shr:2 row_mask:0xf bank_mask:0xf bound_ctrl:1
	v_add_f32_dpp v125, v125, v125 row_shr:2 row_mask:0xf bank_mask:0xf bound_ctrl:1
	s_nop 1
	v_add_f32_dpp v124, v124, v124 row_shr:4 row_mask:0xf bank_mask:0xf bound_ctrl:1
	v_add_f32_dpp v125, v125, v125 row_shr:4 row_mask:0xf bank_mask:0xf bound_ctrl:1
	s_nop 1
	v_add_f32_dpp v124, v124, v124 row_shr:8 row_mask:0xf bank_mask:0xf bound_ctrl:1
	v_add_f32_dpp v125, v125, v125 row_shr:8 row_mask:0xf bank_mask:0xf bound_ctrl:1
	s_nop 0
	v_cvt_pk_f16_f32 v123, v124, v125

.LBB0_738:
	v_pk_mul_f32 v[112:113], v[122:123], s[6:7] op_sel_hi:[1,0]
	s_nop 1
	v_mov_b32_dpp v112, v112 row_shr:1 row_mask:0xf bank_mask:0xf bound_ctrl:1
	v_mov_b32_dpp v113, v113 row_shr:1 row_mask:0xf bank_mask:0xf bound_ctrl:1
	v_pk_fma_f32 v[112:113], v[122:123], s[6:7], v[112:113] op_sel_hi:[1,0,1]
	s_nop 1
	v_add_f32_dpp v112, v112, v112 row_shr:2 row_mask:0xf bank_mask:0xf bound_ctrl:1
	v_add_f32_dpp v113, v113, v113 row_shr:2 row_mask:0xf bank_mask:0xf bound_ctrl:1
	s_nop 1
	v_add_f32_dpp v112, v112, v112 row_shr:4 row_mask:0xf bank_mask:0xf bound_ctrl:1
	v_add_f32_dpp v113, v113, v113 row_shr:4 row_mask:0xf bank_mask:0xf bound_ctrl:1
	s_nop 1
	v_add_f32_dpp v112, v112, v112 row_shr:8 row_mask:0xf bank_mask:0xf bound_ctrl:1
	v_add_f32_dpp v113, v113, v113 row_shr:8 row_mask:0xf bank_mask:0xf bound_ctrl:1
	v_pk_mul_f32 v[114:115], v[120:121], s[6:7] op_sel_hi:[1,0]
	v_cvt_pk_f16_f32 v112, v112, v113
	s_nop 0
	v_mov_b32_dpp v114, v114 row_shr:1 row_mask:0xf bank_mask:0xf bound_ctrl:1
	v_mov_b32_dpp v115, v115 row_shr:1 row_mask:0xf bank_mask:0xf bound_ctrl:1
	v_pk_fma_f32 v[114:115], v[120:121], s[6:7], v[114:115] op_sel_hi:[1,0,1]
	s_nop 1
	v_add_f32_dpp v114, v114, v114 row_shr:2 row_mask:0xf bank_mask:0xf bound_ctrl:1
	v_add_f32_dpp v115, v115, v115 row_shr:2 row_mask:0xf bank_mask:0xf bound_ctrl:1
	s_nop 1
	v_add_f32_dpp v114, v114, v114 row_shr:4 row_mask:0xf bank_mask:0xf bound_ctrl:1
	v_add_f32_dpp v115, v115, v115 row_shr:4 row_mask:0xf bank_mask:0xf bound_ctrl:1
	s_nop 1
	v_add_f32_dpp v114, v114, v114 row_shr:8 row_mask:0xf bank_mask:0xf bound_ctrl:1
	v_add_f32_dpp v115, v115, v115 row_shr:8 row_mask:0xf bank_mask:0xf bound_ctrl:1
	v_pk_mul_f32 v[120:121], v[118:119], s[6:7] op_sel_hi:[1,0]
	v_cvt_pk_f16_f32 v114, v114, v115
	s_nop 0
	v_mov_b32_dpp v120, v120 row_shr:1 row_mask:0xf bank_mask:0xf bound_ctrl:1
	v_mov_b32_dpp v121, v121 row_shr:1 row_mask:0xf bank_mask:0xf bound_ctrl:1
	v_pk_fma_f32 v[118:119], v[118:119], s[6:7], v[120:121] op_sel_hi:[1,0,1]
	s_nop 1
	v_add_f32_dpp v118, v118, v118 row_shr:2 row_mask:0xf bank_mask:0xf bound_ctrl:1
	v_add_f32_dpp v119, v119, v119 row_shr:2 row_mask:0xf bank_mask:0xf bound_ctrl:1
	s_nop 1
	v_add_f32_dpp v118, v118, v118 row_shr:4 row_mask:0xf bank_mask:0xf bound_ctrl:1
	v_add_f32_dpp v119, v119, v119 row_shr:4 row_mask:0xf bank_mask:0xf bound_ctrl:1
	s_nop 1
	v_add_f32_dpp v118, v118, v118 row_shr:8 row_mask:0xf bank_mask:0xf bound_ctrl:1
	v_add_f32_dpp v119, v119, v119 row_shr:8 row_mask:0xf bank_mask:0xf bound_ctrl:1
	v_pk_mul_f32 v[120:121], v[116:117], s[6:7] op_sel_hi:[1,0]
	v_cvt_pk_f16_f32 v113, v118, v119
	s_nop 0
	v_mov_b32_dpp v120, v120 row_shr:1 row_mask:0xf bank_mask:0xf bound_ctrl:1
	v_mov_b32_dpp v121, v121 row_shr:1 row_mask:0xf bank_mask:0xf bound_ctrl:1
	v_pk_fma_f32 v[116:117], v[116:117], s[6:7], v[120:121] op_sel_hi:[1,0,1]
	s_nop 1
	v_add_f32_dpp v116, v116, v116 row_shr:2 row_mask:0xf bank_mask:0xf bound_ctrl:1
	v_add_f32_dpp v117, v117, v117 row_shr:2 row_mask:0xf bank_mask:0xf bound_ctrl:1
	s_nop 1
	v_add_f32_dpp v116, v116, v116 row_shr:4 row_mask:0xf bank_mask:0xf bound_ctrl:1
	v_add_f32_dpp v117, v117, v117 row_shr:4 row_mask:0xf bank_mask:0xf bound_ctrl:1
	s_nop 1
	v_add_f32_dpp v116, v116, v116 row_shr:8 row_mask:0xf bank_mask:0xf bound_ctrl:1
	v_add_f32_dpp v117, v117, v117 row_shr:8 row_mask:0xf bank_mask:0xf bound_ctrl:1
	s_nop 0
	v_cvt_pk_f16_f32 v115, v116, v117

.LBB0_742:
	v_pk_mul_f32 v[104:105], v[114:115], s[6:7] op_sel_hi:[1,0]
	s_nop 1
	v_mov_b32_dpp v104, v104 row_shr:1 row_mask:0xf bank_mask:0xf bound_ctrl:1
	v_mov_b32_dpp v105, v105 row_shr:1 row_mask:0xf bank_mask:0xf bound_ctrl:1
	v_pk_fma_f32 v[104:105], v[114:115], s[6:7], v[104:105] op_sel_hi:[1,0,1]
	s_nop 1
	v_add_f32_dpp v104, v104, v104 row_shr:2 row_mask:0xf bank_mask:0xf bound_ctrl:1
	v_add_f32_dpp v105, v105, v105 row_shr:2 row_mask:0xf bank_mask:0xf bound_ctrl:1
	s_nop 1
	v_add_f32_dpp v104, v104, v104 row_shr:4 row_mask:0xf bank_mask:0xf bound_ctrl:1
	v_add_f32_dpp v105, v105, v105 row_shr:4 row_mask:0xf bank_mask:0xf bound_ctrl:1
	s_nop 1
	v_add_f32_dpp v104, v104, v104 row_shr:8 row_mask:0xf bank_mask:0xf bound_ctrl:1
	v_add_f32_dpp v105, v105, v105 row_shr:8 row_mask:0xf bank_mask:0xf bound_ctrl:1
	v_pk_mul_f32 v[106:107], v[112:113], s[6:7] op_sel_hi:[1,0]
	v_cvt_pk_f16_f32 v104, v104, v105
	s_nop 0
	v_mov_b32_dpp v106, v106 row_shr:1 row_mask:0xf bank_mask:0xf bound_ctrl:1
	v_mov_b32_dpp v107, v107 row_shr:1 row_mask:0xf bank_mask:0xf bound_ctrl:1
	v_pk_fma_f32 v[106:107], v[112:113], s[6:7], v[106:107] op_sel_hi:[1,0,1]
	s_nop 1
	v_add_f32_dpp v106, v106, v106 row_shr:2 row_mask:0xf bank_mask:0xf bound_ctrl:1
	v_add_f32_dpp v107, v107, v107 row_shr:2 row_mask:0xf bank_mask:0xf bound_ctrl:1
	s_nop 1
	v_add_f32_dpp v106, v106, v106 row_shr:4 row_mask:0xf bank_mask:0xf bound_ctrl:1
	v_add_f32_dpp v107, v107, v107 row_shr:4 row_mask:0xf bank_mask:0xf bound_ctrl:1
	s_nop 1
	v_add_f32_dpp v106, v106, v106 row_shr:8 row_mask:0xf bank_mask:0xf bound_ctrl:1
	v_add_f32_dpp v107, v107, v107 row_shr:8 row_mask:0xf bank_mask:0xf bound_ctrl:1
	v_pk_mul_f32 v[112:113], v[110:111], s[6:7] op_sel_hi:[1,0]
	v_cvt_pk_f16_f32 v106, v106, v107
	s_nop 0
	v_mov_b32_dpp v112, v112 row_shr:1 row_mask:0xf bank_mask:0xf bound_ctrl:1
	v_mov_b32_dpp v113, v113 row_shr:1 row_mask:0xf bank_mask:0xf bound_ctrl:1
	v_pk_fma_f32 v[110:111], v[110:111], s[6:7], v[112:113] op_sel_hi:[1,0,1]
	s_nop 1
	v_add_f32_dpp v110, v110, v110 row_shr:2 row_mask:0xf bank_mask:0xf bound_ctrl:1
	v_add_f32_dpp v111, v111, v111 row_shr:2 row_mask:0xf bank_mask:0xf bound_ctrl:1
	s_nop 1
	v_add_f32_dpp v110, v110, v110 row_shr:4 row_mask:0xf bank_mask:0xf bound_ctrl:1
	v_add_f32_dpp v111, v111, v111 row_shr:4 row_mask:0xf bank_mask:0xf bound_ctrl:1
	s_nop 1
	v_add_f32_dpp v110, v110, v110 row_shr:8 row_mask:0xf bank_mask:0xf bound_ctrl:1
	v_add_f32_dpp v111, v111, v111 row_shr:8 row_mask:0xf bank_mask:0xf bound_ctrl:1
	v_pk_mul_f32 v[112:113], v[108:109], s[6:7] op_sel_hi:[1,0]
	v_cvt_pk_f16_f32 v105, v110, v111
	s_nop 0
	v_mov_b32_dpp v112, v112 row_shr:1 row_mask:0xf bank_mask:0xf bound_ctrl:1
	v_mov_b32_dpp v113, v113 row_shr:1 row_mask:0xf bank_mask:0xf bound_ctrl:1
	v_pk_fma_f32 v[108:109], v[108:109], s[6:7], v[112:113] op_sel_hi:[1,0,1]
	s_nop 1
	v_add_f32_dpp v108, v108, v108 row_shr:2 row_mask:0xf bank_mask:0xf bound_ctrl:1
	v_add_f32_dpp v109, v109, v109 row_shr:2 row_mask:0xf bank_mask:0xf bound_ctrl:1
	s_nop 1
	v_add_f32_dpp v108, v108, v108 row_shr:4 row_mask:0xf bank_mask:0xf bound_ctrl:1
	v_add_f32_dpp v109, v109, v109 row_shr:4 row_mask:0xf bank_mask:0xf bound_ctrl:1
	s_nop 1
	v_add_f32_dpp v108, v108, v108 row_shr:8 row_mask:0xf bank_mask:0xf bound_ctrl:1
	v_add_f32_dpp v109, v109, v109 row_shr:8 row_mask:0xf bank_mask:0xf bound_ctrl:1
	s_nop 0
	v_cvt_pk_f16_f32 v107, v108, v109

.LBB0_746:
	v_pk_mul_f32 v[96:97], v[106:107], s[6:7] op_sel_hi:[1,0]
	s_nop 1
	v_mov_b32_dpp v96, v96 row_shr:1 row_mask:0xf bank_mask:0xf bound_ctrl:1
	v_mov_b32_dpp v97, v97 row_shr:1 row_mask:0xf bank_mask:0xf bound_ctrl:1
	v_pk_fma_f32 v[96:97], v[106:107], s[6:7], v[96:97] op_sel_hi:[1,0,1]
	s_nop 1
	v_add_f32_dpp v96, v96, v96 row_shr:2 row_mask:0xf bank_mask:0xf bound_ctrl:1
	v_add_f32_dpp v97, v97, v97 row_shr:2 row_mask:0xf bank_mask:0xf bound_ctrl:1
	s_nop 1
	v_add_f32_dpp v96, v96, v96 row_shr:4 row_mask:0xf bank_mask:0xf bound_ctrl:1
	v_add_f32_dpp v97, v97, v97 row_shr:4 row_mask:0xf bank_mask:0xf bound_ctrl:1
	s_nop 1
	v_add_f32_dpp v96, v96, v96 row_shr:8 row_mask:0xf bank_mask:0xf bound_ctrl:1
	v_add_f32_dpp v97, v97, v97 row_shr:8 row_mask:0xf bank_mask:0xf bound_ctrl:1
	v_pk_mul_f32 v[98:99], v[104:105], s[6:7] op_sel_hi:[1,0]
	v_cvt_pk_f16_f32 v96, v96, v97
	s_nop 0
	v_mov_b32_dpp v98, v98 row_shr:1 row_mask:0xf bank_mask:0xf bound_ctrl:1
	v_mov_b32_dpp v99, v99 row_shr:1 row_mask:0xf bank_mask:0xf bound_ctrl:1
	v_pk_fma_f32 v[98:99], v[104:105], s[6:7], v[98:99] op_sel_hi:[1,0,1]
	s_nop 1
	v_add_f32_dpp v98, v98, v98 row_shr:2 row_mask:0xf bank_mask:0xf bound_ctrl:1
	v_add_f32_dpp v99, v99, v99 row_shr:2 row_mask:0xf bank_mask:0xf bound_ctrl:1
	s_nop 1
	v_add_f32_dpp v98, v98, v98 row_shr:4 row_mask:0xf bank_mask:0xf bound_ctrl:1
	v_add_f32_dpp v99, v99, v99 row_shr:4 row_mask:0xf bank_mask:0xf bound_ctrl:1
	s_nop 1
	v_add_f32_dpp v98, v98, v98 row_shr:8 row_mask:0xf bank_mask:0xf bound_ctrl:1
	v_add_f32_dpp v99, v99, v99 row_shr:8 row_mask:0xf bank_mask:0xf bound_ctrl:1
	v_pk_mul_f32 v[104:105], v[102:103], s[6:7] op_sel_hi:[1,0]
	v_cvt_pk_f16_f32 v98, v98, v99
	s_nop 0
	v_mov_b32_dpp v104, v104 row_shr:1 row_mask:0xf bank_mask:0xf bound_ctrl:1
	v_mov_b32_dpp v105, v105 row_shr:1 row_mask:0xf bank_mask:0xf bound_ctrl:1
	v_pk_fma_f32 v[102:103], v[102:103], s[6:7], v[104:105] op_sel_hi:[1,0,1]
	s_nop 1
	v_add_f32_dpp v102, v102, v102 row_shr:2 row_mask:0xf bank_mask:0xf bound_ctrl:1
	v_add_f32_dpp v103, v103, v103 row_shr:2 row_mask:0xf bank_mask:0xf bound_ctrl:1
	s_nop 1
	v_add_f32_dpp v102, v102, v102 row_shr:4 row_mask:0xf bank_mask:0xf bound_ctrl:1
	v_add_f32_dpp v103, v103, v103 row_shr:4 row_mask:0xf bank_mask:0xf bound_ctrl:1
	s_nop 1
	v_add_f32_dpp v102, v102, v102 row_shr:8 row_mask:0xf bank_mask:0xf bound_ctrl:1
	v_add_f32_dpp v103, v103, v103 row_shr:8 row_mask:0xf bank_mask:0xf bound_ctrl:1
	v_pk_mul_f32 v[104:105], v[100:101], s[6:7] op_sel_hi:[1,0]
	v_cvt_pk_f16_f32 v97, v102, v103
	s_nop 0
	v_mov_b32_dpp v104, v104 row_shr:1 row_mask:0xf bank_mask:0xf bound_ctrl:1
	v_mov_b32_dpp v105, v105 row_shr:1 row_mask:0xf bank_mask:0xf bound_ctrl:1
	v_pk_fma_f32 v[100:101], v[100:101], s[6:7], v[104:105] op_sel_hi:[1,0,1]
	s_nop 1
	v_add_f32_dpp v100, v100, v100 row_shr:2 row_mask:0xf bank_mask:0xf bound_ctrl:1
	v_add_f32_dpp v101, v101, v101 row_shr:2 row_mask:0xf bank_mask:0xf bound_ctrl:1
	s_nop 1
	v_add_f32_dpp v100, v100, v100 row_shr:4 row_mask:0xf bank_mask:0xf bound_ctrl:1
	v_add_f32_dpp v101, v101, v101 row_shr:4 row_mask:0xf bank_mask:0xf bound_ctrl:1
	s_nop 1
	v_add_f32_dpp v100, v100, v100 row_shr:8 row_mask:0xf bank_mask:0xf bound_ctrl:1
	v_add_f32_dpp v101, v101, v101 row_shr:8 row_mask:0xf bank_mask:0xf bound_ctrl:1
	s_nop 0
	v_cvt_pk_f16_f32 v99, v100, v101

.LBB0_750:
	v_pk_mul_f32 v[88:89], v[98:99], s[6:7] op_sel_hi:[1,0]
	s_nop 1
	v_mov_b32_dpp v88, v88 row_shr:1 row_mask:0xf bank_mask:0xf bound_ctrl:1
	v_mov_b32_dpp v89, v89 row_shr:1 row_mask:0xf bank_mask:0xf bound_ctrl:1
	v_pk_fma_f32 v[88:89], v[98:99], s[6:7], v[88:89] op_sel_hi:[1,0,1]
	s_nop 1
	v_add_f32_dpp v88, v88, v88 row_shr:2 row_mask:0xf bank_mask:0xf bound_ctrl:1
	v_add_f32_dpp v89, v89, v89 row_shr:2 row_mask:0xf bank_mask:0xf bound_ctrl:1
	s_nop 1
	v_add_f32_dpp v88, v88, v88 row_shr:4 row_mask:0xf bank_mask:0xf bound_ctrl:1
	v_add_f32_dpp v89, v89, v89 row_shr:4 row_mask:0xf bank_mask:0xf bound_ctrl:1
	s_nop 1
	v_add_f32_dpp v88, v88, v88 row_shr:8 row_mask:0xf bank_mask:0xf bound_ctrl:1
	v_add_f32_dpp v89, v89, v89 row_shr:8 row_mask:0xf bank_mask:0xf bound_ctrl:1
	v_pk_mul_f32 v[90:91], v[96:97], s[6:7] op_sel_hi:[1,0]
	v_cvt_pk_f16_f32 v88, v88, v89
	s_nop 0
	v_mov_b32_dpp v90, v90 row_shr:1 row_mask:0xf bank_mask:0xf bound_ctrl:1
	v_mov_b32_dpp v91, v91 row_shr:1 row_mask:0xf bank_mask:0xf bound_ctrl:1
	v_pk_fma_f32 v[90:91], v[96:97], s[6:7], v[90:91] op_sel_hi:[1,0,1]
	s_nop 1
	v_add_f32_dpp v90, v90, v90 row_shr:2 row_mask:0xf bank_mask:0xf bound_ctrl:1
	v_add_f32_dpp v91, v91, v91 row_shr:2 row_mask:0xf bank_mask:0xf bound_ctrl:1
	s_nop 1
	v_add_f32_dpp v90, v90, v90 row_shr:4 row_mask:0xf bank_mask:0xf bound_ctrl:1
	v_add_f32_dpp v91, v91, v91 row_shr:4 row_mask:0xf bank_mask:0xf bound_ctrl:1
	s_nop 1
	v_add_f32_dpp v90, v90, v90 row_shr:8 row_mask:0xf bank_mask:0xf bound_ctrl:1
	v_add_f32_dpp v91, v91, v91 row_shr:8 row_mask:0xf bank_mask:0xf bound_ctrl:1
	v_pk_mul_f32 v[96:97], v[94:95], s[6:7] op_sel_hi:[1,0]
	v_cvt_pk_f16_f32 v90, v90, v91
	s_nop 0
	v_mov_b32_dpp v96, v96 row_shr:1 row_mask:0xf bank_mask:0xf bound_ctrl:1
	v_mov_b32_dpp v97, v97 row_shr:1 row_mask:0xf bank_mask:0xf bound_ctrl:1
	v_pk_fma_f32 v[94:95], v[94:95], s[6:7], v[96:97] op_sel_hi:[1,0,1]
	s_nop 1
	v_add_f32_dpp v94, v94, v94 row_shr:2 row_mask:0xf bank_mask:0xf bound_ctrl:1
	v_add_f32_dpp v95, v95, v95 row_shr:2 row_mask:0xf bank_mask:0xf bound_ctrl:1
	s_nop 1
	v_add_f32_dpp v94, v94, v94 row_shr:4 row_mask:0xf bank_mask:0xf bound_ctrl:1
	v_add_f32_dpp v95, v95, v95 row_shr:4 row_mask:0xf bank_mask:0xf bound_ctrl:1
	s_nop 1
	v_add_f32_dpp v94, v94, v94 row_shr:8 row_mask:0xf bank_mask:0xf bound_ctrl:1
	v_add_f32_dpp v95, v95, v95 row_shr:8 row_mask:0xf bank_mask:0xf bound_ctrl:1
	v_pk_mul_f32 v[96:97], v[92:93], s[6:7] op_sel_hi:[1,0]
	v_cvt_pk_f16_f32 v89, v94, v95
	s_nop 0
	v_mov_b32_dpp v96, v96 row_shr:1 row_mask:0xf bank_mask:0xf bound_ctrl:1
	v_mov_b32_dpp v97, v97 row_shr:1 row_mask:0xf bank_mask:0xf bound_ctrl:1
	v_pk_fma_f32 v[92:93], v[92:93], s[6:7], v[96:97] op_sel_hi:[1,0,1]
	s_nop 1
	v_add_f32_dpp v92, v92, v92 row_shr:2 row_mask:0xf bank_mask:0xf bound_ctrl:1
	v_add_f32_dpp v93, v93, v93 row_shr:2 row_mask:0xf bank_mask:0xf bound_ctrl:1
	s_nop 1
	v_add_f32_dpp v92, v92, v92 row_shr:4 row_mask:0xf bank_mask:0xf bound_ctrl:1
	v_add_f32_dpp v93, v93, v93 row_shr:4 row_mask:0xf bank_mask:0xf bound_ctrl:1
	s_nop 1
	v_add_f32_dpp v92, v92, v92 row_shr:8 row_mask:0xf bank_mask:0xf bound_ctrl:1
	v_add_f32_dpp v93, v93, v93 row_shr:8 row_mask:0xf bank_mask:0xf bound_ctrl:1
	s_nop 0
	v_cvt_pk_f16_f32 v91, v92, v93

.LBB0_754:
	v_pk_mul_f32 v[80:81], v[90:91], s[6:7] op_sel_hi:[1,0]
	s_nop 1
	v_mov_b32_dpp v80, v80 row_shr:1 row_mask:0xf bank_mask:0xf bound_ctrl:1
	v_mov_b32_dpp v81, v81 row_shr:1 row_mask:0xf bank_mask:0xf bound_ctrl:1
	v_pk_fma_f32 v[80:81], v[90:91], s[6:7], v[80:81] op_sel_hi:[1,0,1]
	s_nop 1
	v_add_f32_dpp v80, v80, v80 row_shr:2 row_mask:0xf bank_mask:0xf bound_ctrl:1
	v_add_f32_dpp v81, v81, v81 row_shr:2 row_mask:0xf bank_mask:0xf bound_ctrl:1
	s_nop 1
	v_add_f32_dpp v80, v80, v80 row_shr:4 row_mask:0xf bank_mask:0xf bound_ctrl:1
	v_add_f32_dpp v81, v81, v81 row_shr:4 row_mask:0xf bank_mask:0xf bound_ctrl:1
	s_nop 1
	v_add_f32_dpp v80, v80, v80 row_shr:8 row_mask:0xf bank_mask:0xf bound_ctrl:1
	v_add_f32_dpp v81, v81, v81 row_shr:8 row_mask:0xf bank_mask:0xf bound_ctrl:1
	v_pk_mul_f32 v[82:83], v[88:89], s[6:7] op_sel_hi:[1,0]
	v_cvt_pk_f16_f32 v80, v80, v81
	s_nop 0
	v_mov_b32_dpp v82, v82 row_shr:1 row_mask:0xf bank_mask:0xf bound_ctrl:1
	v_mov_b32_dpp v83, v83 row_shr:1 row_mask:0xf bank_mask:0xf bound_ctrl:1
	v_pk_fma_f32 v[82:83], v[88:89], s[6:7], v[82:83] op_sel_hi:[1,0,1]
	s_nop 1
	v_add_f32_dpp v82, v82, v82 row_shr:2 row_mask:0xf bank_mask:0xf bound_ctrl:1
	v_add_f32_dpp v83, v83, v83 row_shr:2 row_mask:0xf bank_mask:0xf bound_ctrl:1
	s_nop 1
	v_add_f32_dpp v82, v82, v82 row_shr:4 row_mask:0xf bank_mask:0xf bound_ctrl:1
	v_add_f32_dpp v83, v83, v83 row_shr:4 row_mask:0xf bank_mask:0xf bound_ctrl:1
	s_nop 1
	v_add_f32_dpp v82, v82, v82 row_shr:8 row_mask:0xf bank_mask:0xf bound_ctrl:1
	v_add_f32_dpp v83, v83, v83 row_shr:8 row_mask:0xf bank_mask:0xf bound_ctrl:1
	v_pk_mul_f32 v[88:89], v[86:87], s[6:7] op_sel_hi:[1,0]
	v_cvt_pk_f16_f32 v82, v82, v83
	s_nop 0
	v_mov_b32_dpp v88, v88 row_shr:1 row_mask:0xf bank_mask:0xf bound_ctrl:1
	v_mov_b32_dpp v89, v89 row_shr:1 row_mask:0xf bank_mask:0xf bound_ctrl:1
	v_pk_fma_f32 v[86:87], v[86:87], s[6:7], v[88:89] op_sel_hi:[1,0,1]
	s_nop 1
	v_add_f32_dpp v86, v86, v86 row_shr:2 row_mask:0xf bank_mask:0xf bound_ctrl:1
	v_add_f32_dpp v87, v87, v87 row_shr:2 row_mask:0xf bank_mask:0xf bound_ctrl:1
	s_nop 1
	v_add_f32_dpp v86, v86, v86 row_shr:4 row_mask:0xf bank_mask:0xf bound_ctrl:1
	v_add_f32_dpp v87, v87, v87 row_shr:4 row_mask:0xf bank_mask:0xf bound_ctrl:1
	s_nop 1
	v_add_f32_dpp v86, v86, v86 row_shr:8 row_mask:0xf bank_mask:0xf bound_ctrl:1
	v_add_f32_dpp v87, v87, v87 row_shr:8 row_mask:0xf bank_mask:0xf bound_ctrl:1
	v_pk_mul_f32 v[88:89], v[84:85], s[6:7] op_sel_hi:[1,0]
	v_cvt_pk_f16_f32 v81, v86, v87
	s_nop 0
	v_mov_b32_dpp v88, v88 row_shr:1 row_mask:0xf bank_mask:0xf bound_ctrl:1
	v_mov_b32_dpp v89, v89 row_shr:1 row_mask:0xf bank_mask:0xf bound_ctrl:1
	v_pk_fma_f32 v[84:85], v[84:85], s[6:7], v[88:89] op_sel_hi:[1,0,1]
	s_nop 1
	v_add_f32_dpp v84, v84, v84 row_shr:2 row_mask:0xf bank_mask:0xf bound_ctrl:1
	v_add_f32_dpp v85, v85, v85 row_shr:2 row_mask:0xf bank_mask:0xf bound_ctrl:1
	s_nop 1
	v_add_f32_dpp v84, v84, v84 row_shr:4 row_mask:0xf bank_mask:0xf bound_ctrl:1
	v_add_f32_dpp v85, v85, v85 row_shr:4 row_mask:0xf bank_mask:0xf bound_ctrl:1
	s_nop 1
	v_add_f32_dpp v84, v84, v84 row_shr:8 row_mask:0xf bank_mask:0xf bound_ctrl:1
	v_add_f32_dpp v85, v85, v85 row_shr:8 row_mask:0xf bank_mask:0xf bound_ctrl:1
	s_nop 0
	v_cvt_pk_f16_f32 v83, v84, v85

.LBB0_758:
	v_pk_mul_f32 v[72:73], v[82:83], s[6:7] op_sel_hi:[1,0]
	s_nop 1
	v_mov_b32_dpp v72, v72 row_shr:1 row_mask:0xf bank_mask:0xf bound_ctrl:1
	v_mov_b32_dpp v73, v73 row_shr:1 row_mask:0xf bank_mask:0xf bound_ctrl:1
	v_pk_fma_f32 v[72:73], v[82:83], s[6:7], v[72:73] op_sel_hi:[1,0,1]
	s_nop 1
	v_add_f32_dpp v72, v72, v72 row_shr:2 row_mask:0xf bank_mask:0xf bound_ctrl:1
	v_add_f32_dpp v73, v73, v73 row_shr:2 row_mask:0xf bank_mask:0xf bound_ctrl:1
	s_nop 1
	v_add_f32_dpp v72, v72, v72 row_shr:4 row_mask:0xf bank_mask:0xf bound_ctrl:1
	v_add_f32_dpp v73, v73, v73 row_shr:4 row_mask:0xf bank_mask:0xf bound_ctrl:1
	s_nop 1
	v_add_f32_dpp v72, v72, v72 row_shr:8 row_mask:0xf bank_mask:0xf bound_ctrl:1
	v_add_f32_dpp v73, v73, v73 row_shr:8 row_mask:0xf bank_mask:0xf bound_ctrl:1
	v_pk_mul_f32 v[74:75], v[80:81], s[6:7] op_sel_hi:[1,0]
	v_cvt_pk_f16_f32 v72, v72, v73
	s_nop 0
	v_mov_b32_dpp v74, v74 row_shr:1 row_mask:0xf bank_mask:0xf bound_ctrl:1
	v_mov_b32_dpp v75, v75 row_shr:1 row_mask:0xf bank_mask:0xf bound_ctrl:1
	v_pk_fma_f32 v[74:75], v[80:81], s[6:7], v[74:75] op_sel_hi:[1,0,1]
	s_nop 1
	v_add_f32_dpp v74, v74, v74 row_shr:2 row_mask:0xf bank_mask:0xf bound_ctrl:1
	v_add_f32_dpp v75, v75, v75 row_shr:2 row_mask:0xf bank_mask:0xf bound_ctrl:1
	s_nop 1
	v_add_f32_dpp v74, v74, v74 row_shr:4 row_mask:0xf bank_mask:0xf bound_ctrl:1
	v_add_f32_dpp v75, v75, v75 row_shr:4 row_mask:0xf bank_mask:0xf bound_ctrl:1
	s_nop 1
	v_add_f32_dpp v74, v74, v74 row_shr:8 row_mask:0xf bank_mask:0xf bound_ctrl:1
	v_add_f32_dpp v75, v75, v75 row_shr:8 row_mask:0xf bank_mask:0xf bound_ctrl:1
	v_pk_mul_f32 v[80:81], v[78:79], s[6:7] op_sel_hi:[1,0]
	v_cvt_pk_f16_f32 v74, v74, v75
	s_nop 0
	v_mov_b32_dpp v80, v80 row_shr:1 row_mask:0xf bank_mask:0xf bound_ctrl:1
	v_mov_b32_dpp v81, v81 row_shr:1 row_mask:0xf bank_mask:0xf bound_ctrl:1
	v_pk_fma_f32 v[78:79], v[78:79], s[6:7], v[80:81] op_sel_hi:[1,0,1]
	s_nop 1
	v_add_f32_dpp v78, v78, v78 row_shr:2 row_mask:0xf bank_mask:0xf bound_ctrl:1
	v_add_f32_dpp v79, v79, v79 row_shr:2 row_mask:0xf bank_mask:0xf bound_ctrl:1
	s_nop 1
	v_add_f32_dpp v78, v78, v78 row_shr:4 row_mask:0xf bank_mask:0xf bound_ctrl:1
	v_add_f32_dpp v79, v79, v79 row_shr:4 row_mask:0xf bank_mask:0xf bound_ctrl:1
	s_nop 1
	v_add_f32_dpp v78, v78, v78 row_shr:8 row_mask:0xf bank_mask:0xf bound_ctrl:1
	v_add_f32_dpp v79, v79, v79 row_shr:8 row_mask:0xf bank_mask:0xf bound_ctrl:1
	v_pk_mul_f32 v[80:81], v[76:77], s[6:7] op_sel_hi:[1,0]
	v_cvt_pk_f16_f32 v73, v78, v79
	s_nop 0
	v_mov_b32_dpp v80, v80 row_shr:1 row_mask:0xf bank_mask:0xf bound_ctrl:1
	v_mov_b32_dpp v81, v81 row_shr:1 row_mask:0xf bank_mask:0xf bound_ctrl:1
	v_pk_fma_f32 v[76:77], v[76:77], s[6:7], v[80:81] op_sel_hi:[1,0,1]
	s_nop 1
	v_add_f32_dpp v76, v76, v76 row_shr:2 row_mask:0xf bank_mask:0xf bound_ctrl:1
	v_add_f32_dpp v77, v77, v77 row_shr:2 row_mask:0xf bank_mask:0xf bound_ctrl:1
	s_nop 1
	v_add_f32_dpp v76, v76, v76 row_shr:4 row_mask:0xf bank_mask:0xf bound_ctrl:1
	v_add_f32_dpp v77, v77, v77 row_shr:4 row_mask:0xf bank_mask:0xf bound_ctrl:1
	s_nop 1
	v_add_f32_dpp v76, v76, v76 row_shr:8 row_mask:0xf bank_mask:0xf bound_ctrl:1
	v_add_f32_dpp v77, v77, v77 row_shr:8 row_mask:0xf bank_mask:0xf bound_ctrl:1
	s_nop 0
	v_cvt_pk_f16_f32 v75, v76, v77

.LBB0_762:
	v_pk_mul_f32 v[64:65], v[74:75], s[6:7] op_sel_hi:[1,0]
	s_nop 1
	v_mov_b32_dpp v64, v64 row_shr:1 row_mask:0xf bank_mask:0xf bound_ctrl:1
	v_mov_b32_dpp v65, v65 row_shr:1 row_mask:0xf bank_mask:0xf bound_ctrl:1
	v_pk_fma_f32 v[64:65], v[74:75], s[6:7], v[64:65] op_sel_hi:[1,0,1]
	s_nop 1
	v_add_f32_dpp v64, v64, v64 row_shr:2 row_mask:0xf bank_mask:0xf bound_ctrl:1
	v_add_f32_dpp v65, v65, v65 row_shr:2 row_mask:0xf bank_mask:0xf bound_ctrl:1
	s_nop 1
	v_add_f32_dpp v64, v64, v64 row_shr:4 row_mask:0xf bank_mask:0xf bound_ctrl:1
	v_add_f32_dpp v65, v65, v65 row_shr:4 row_mask:0xf bank_mask:0xf bound_ctrl:1
	s_nop 1
	v_add_f32_dpp v64, v64, v64 row_shr:8 row_mask:0xf bank_mask:0xf bound_ctrl:1
	v_add_f32_dpp v65, v65, v65 row_shr:8 row_mask:0xf bank_mask:0xf bound_ctrl:1
	v_pk_mul_f32 v[66:67], v[72:73], s[6:7] op_sel_hi:[1,0]
	v_cvt_pk_f16_f32 v64, v64, v65
	s_nop 0
	v_mov_b32_dpp v66, v66 row_shr:1 row_mask:0xf bank_mask:0xf bound_ctrl:1
	v_mov_b32_dpp v67, v67 row_shr:1 row_mask:0xf bank_mask:0xf bound_ctrl:1
	v_pk_fma_f32 v[66:67], v[72:73], s[6:7], v[66:67] op_sel_hi:[1,0,1]
	s_nop 1
	v_add_f32_dpp v66, v66, v66 row_shr:2 row_mask:0xf bank_mask:0xf bound_ctrl:1
	v_add_f32_dpp v67, v67, v67 row_shr:2 row_mask:0xf bank_mask:0xf bound_ctrl:1
	s_nop 1
	v_add_f32_dpp v66, v66, v66 row_shr:4 row_mask:0xf bank_mask:0xf bound_ctrl:1
	v_add_f32_dpp v67, v67, v67 row_shr:4 row_mask:0xf bank_mask:0xf bound_ctrl:1
	s_nop 1
	v_add_f32_dpp v66, v66, v66 row_shr:8 row_mask:0xf bank_mask:0xf bound_ctrl:1
	v_add_f32_dpp v67, v67, v67 row_shr:8 row_mask:0xf bank_mask:0xf bound_ctrl:1
	v_pk_mul_f32 v[72:73], v[70:71], s[6:7] op_sel_hi:[1,0]
	v_cvt_pk_f16_f32 v66, v66, v67
	s_nop 0
	v_mov_b32_dpp v72, v72 row_shr:1 row_mask:0xf bank_mask:0xf bound_ctrl:1
	v_mov_b32_dpp v73, v73 row_shr:1 row_mask:0xf bank_mask:0xf bound_ctrl:1
	v_pk_fma_f32 v[70:71], v[70:71], s[6:7], v[72:73] op_sel_hi:[1,0,1]
	s_nop 1
	v_add_f32_dpp v70, v70, v70 row_shr:2 row_mask:0xf bank_mask:0xf bound_ctrl:1
	v_add_f32_dpp v71, v71, v71 row_shr:2 row_mask:0xf bank_mask:0xf bound_ctrl:1
	s_nop 1
	v_add_f32_dpp v70, v70, v70 row_shr:4 row_mask:0xf bank_mask:0xf bound_ctrl:1
	v_add_f32_dpp v71, v71, v71 row_shr:4 row_mask:0xf bank_mask:0xf bound_ctrl:1
	s_nop 1
	v_add_f32_dpp v70, v70, v70 row_shr:8 row_mask:0xf bank_mask:0xf bound_ctrl:1
	v_add_f32_dpp v71, v71, v71 row_shr:8 row_mask:0xf bank_mask:0xf bound_ctrl:1
	v_pk_mul_f32 v[72:73], v[68:69], s[6:7] op_sel_hi:[1,0]
	v_cvt_pk_f16_f32 v65, v70, v71
	s_nop 0
	v_mov_b32_dpp v72, v72 row_shr:1 row_mask:0xf bank_mask:0xf bound_ctrl:1
	v_mov_b32_dpp v73, v73 row_shr:1 row_mask:0xf bank_mask:0xf bound_ctrl:1
	v_pk_fma_f32 v[68:69], v[68:69], s[6:7], v[72:73] op_sel_hi:[1,0,1]
	s_nop 1
	v_add_f32_dpp v68, v68, v68 row_shr:2 row_mask:0xf bank_mask:0xf bound_ctrl:1
	v_add_f32_dpp v69, v69, v69 row_shr:2 row_mask:0xf bank_mask:0xf bound_ctrl:1
	s_nop 1
	v_add_f32_dpp v68, v68, v68 row_shr:4 row_mask:0xf bank_mask:0xf bound_ctrl:1
	v_add_f32_dpp v69, v69, v69 row_shr:4 row_mask:0xf bank_mask:0xf bound_ctrl:1
	s_nop 1
	v_add_f32_dpp v68, v68, v68 row_shr:8 row_mask:0xf bank_mask:0xf bound_ctrl:1
	v_add_f32_dpp v69, v69, v69 row_shr:8 row_mask:0xf bank_mask:0xf bound_ctrl:1
	s_nop 0
	v_cvt_pk_f16_f32 v67, v68, v69

.LBB0_766:
	v_pk_mul_f32 v[48:49], v[66:67], s[6:7] op_sel_hi:[1,0]
	s_nop 1
	v_mov_b32_dpp v48, v48 row_shr:1 row_mask:0xf bank_mask:0xf bound_ctrl:1
	v_mov_b32_dpp v49, v49 row_shr:1 row_mask:0xf bank_mask:0xf bound_ctrl:1
	v_pk_fma_f32 v[48:49], v[66:67], s[6:7], v[48:49] op_sel_hi:[1,0,1]
	s_nop 1
	v_add_f32_dpp v48, v48, v48 row_shr:2 row_mask:0xf bank_mask:0xf bound_ctrl:1
	v_add_f32_dpp v49, v49, v49 row_shr:2 row_mask:0xf bank_mask:0xf bound_ctrl:1
	s_nop 1
	v_add_f32_dpp v48, v48, v48 row_shr:4 row_mask:0xf bank_mask:0xf bound_ctrl:1
	v_add_f32_dpp v49, v49, v49 row_shr:4 row_mask:0xf bank_mask:0xf bound_ctrl:1
	s_nop 1
	v_add_f32_dpp v48, v48, v48 row_shr:8 row_mask:0xf bank_mask:0xf bound_ctrl:1
	v_add_f32_dpp v49, v49, v49 row_shr:8 row_mask:0xf bank_mask:0xf bound_ctrl:1
	v_pk_mul_f32 v[50:51], v[64:65], s[6:7] op_sel_hi:[1,0]
	v_cvt_pk_f16_f32 v48, v48, v49
	s_nop 0
	v_mov_b32_dpp v50, v50 row_shr:1 row_mask:0xf bank_mask:0xf bound_ctrl:1
	v_mov_b32_dpp v51, v51 row_shr:1 row_mask:0xf bank_mask:0xf bound_ctrl:1
	v_pk_fma_f32 v[50:51], v[64:65], s[6:7], v[50:51] op_sel_hi:[1,0,1]
	s_nop 1
	v_add_f32_dpp v50, v50, v50 row_shr:2 row_mask:0xf bank_mask:0xf bound_ctrl:1
	v_add_f32_dpp v51, v51, v51 row_shr:2 row_mask:0xf bank_mask:0xf bound_ctrl:1
	s_nop 1
	v_add_f32_dpp v50, v50, v50 row_shr:4 row_mask:0xf bank_mask:0xf bound_ctrl:1
	v_add_f32_dpp v51, v51, v51 row_shr:4 row_mask:0xf bank_mask:0xf bound_ctrl:1
	s_nop 1
	v_add_f32_dpp v50, v50, v50 row_shr:8 row_mask:0xf bank_mask:0xf bound_ctrl:1
	v_add_f32_dpp v51, v51, v51 row_shr:8 row_mask:0xf bank_mask:0xf bound_ctrl:1
	v_pk_mul_f32 v[64:65], v[54:55], s[6:7] op_sel_hi:[1,0]
	v_cvt_pk_f16_f32 v50, v50, v51
	s_nop 0
	v_mov_b32_dpp v64, v64 row_shr:1 row_mask:0xf bank_mask:0xf bound_ctrl:1
	v_mov_b32_dpp v65, v65 row_shr:1 row_mask:0xf bank_mask:0xf bound_ctrl:1
	v_pk_fma_f32 v[54:55], v[54:55], s[6:7], v[64:65] op_sel_hi:[1,0,1]
	s_nop 1
	v_add_f32_dpp v54, v54, v54 row_shr:2 row_mask:0xf bank_mask:0xf bound_ctrl:1
	v_add_f32_dpp v55, v55, v55 row_shr:2 row_mask:0xf bank_mask:0xf bound_ctrl:1
	s_nop 1
	v_add_f32_dpp v54, v54, v54 row_shr:4 row_mask:0xf bank_mask:0xf bound_ctrl:1
	v_add_f32_dpp v55, v55, v55 row_shr:4 row_mask:0xf bank_mask:0xf bound_ctrl:1
	s_nop 1
	v_add_f32_dpp v54, v54, v54 row_shr:8 row_mask:0xf bank_mask:0xf bound_ctrl:1
	v_add_f32_dpp v55, v55, v55 row_shr:8 row_mask:0xf bank_mask:0xf bound_ctrl:1
	v_pk_mul_f32 v[64:65], v[52:53], s[6:7] op_sel_hi:[1,0]
	v_cvt_pk_f16_f32 v49, v54, v55
	s_nop 0
	v_mov_b32_dpp v64, v64 row_shr:1 row_mask:0xf bank_mask:0xf bound_ctrl:1
	v_mov_b32_dpp v65, v65 row_shr:1 row_mask:0xf bank_mask:0xf bound_ctrl:1
	v_pk_fma_f32 v[52:53], v[52:53], s[6:7], v[64:65] op_sel_hi:[1,0,1]
	s_nop 1
	v_add_f32_dpp v52, v52, v52 row_shr:2 row_mask:0xf bank_mask:0xf bound_ctrl:1
	v_add_f32_dpp v53, v53, v53 row_shr:2 row_mask:0xf bank_mask:0xf bound_ctrl:1
	s_nop 1
	v_add_f32_dpp v52, v52, v52 row_shr:4 row_mask:0xf bank_mask:0xf bound_ctrl:1
	v_add_f32_dpp v53, v53, v53 row_shr:4 row_mask:0xf bank_mask:0xf bound_ctrl:1
	s_nop 1
	v_add_f32_dpp v52, v52, v52 row_shr:8 row_mask:0xf bank_mask:0xf bound_ctrl:1
	v_add_f32_dpp v53, v53, v53 row_shr:8 row_mask:0xf bank_mask:0xf bound_ctrl:1
	s_nop 0
	v_cvt_pk_f16_f32 v51, v52, v53

.LBB0_770:
	v_pk_mul_f32 v[32:33], v[50:51], s[6:7] op_sel_hi:[1,0]
	s_nop 1
	v_mov_b32_dpp v32, v32 row_shr:1 row_mask:0xf bank_mask:0xf bound_ctrl:1
	v_mov_b32_dpp v33, v33 row_shr:1 row_mask:0xf bank_mask:0xf bound_ctrl:1
	v_pk_fma_f32 v[32:33], v[50:51], s[6:7], v[32:33] op_sel_hi:[1,0,1]
	s_nop 1
	v_add_f32_dpp v32, v32, v32 row_shr:2 row_mask:0xf bank_mask:0xf bound_ctrl:1
	v_add_f32_dpp v33, v33, v33 row_shr:2 row_mask:0xf bank_mask:0xf bound_ctrl:1
	s_nop 1
	v_add_f32_dpp v32, v32, v32 row_shr:4 row_mask:0xf bank_mask:0xf bound_ctrl:1
	v_add_f32_dpp v33, v33, v33 row_shr:4 row_mask:0xf bank_mask:0xf bound_ctrl:1
	s_nop 1
	v_add_f32_dpp v32, v32, v32 row_shr:8 row_mask:0xf bank_mask:0xf bound_ctrl:1
	v_add_f32_dpp v33, v33, v33 row_shr:8 row_mask:0xf bank_mask:0xf bound_ctrl:1
	v_pk_mul_f32 v[34:35], v[48:49], s[6:7] op_sel_hi:[1,0]
	v_cvt_pk_f16_f32 v32, v32, v33
	s_nop 0
	v_mov_b32_dpp v34, v34 row_shr:1 row_mask:0xf bank_mask:0xf bound_ctrl:1
	v_mov_b32_dpp v35, v35 row_shr:1 row_mask:0xf bank_mask:0xf bound_ctrl:1
	v_pk_fma_f32 v[34:35], v[48:49], s[6:7], v[34:35] op_sel_hi:[1,0,1]
	s_nop 1
	v_add_f32_dpp v34, v34, v34 row_shr:2 row_mask:0xf bank_mask:0xf bound_ctrl:1
	v_add_f32_dpp v35, v35, v35 row_shr:2 row_mask:0xf bank_mask:0xf bound_ctrl:1
	s_nop 1
	v_add_f32_dpp v34, v34, v34 row_shr:4 row_mask:0xf bank_mask:0xf bound_ctrl:1
	v_add_f32_dpp v35, v35, v35 row_shr:4 row_mask:0xf bank_mask:0xf bound_ctrl:1
	s_nop 1
	v_add_f32_dpp v34, v34, v34 row_shr:8 row_mask:0xf bank_mask:0xf bound_ctrl:1
	v_add_f32_dpp v35, v35, v35 row_shr:8 row_mask:0xf bank_mask:0xf bound_ctrl:1
	v_pk_mul_f32 v[48:49], v[38:39], s[6:7] op_sel_hi:[1,0]
	v_cvt_pk_f16_f32 v34, v34, v35
	s_nop 0
	v_mov_b32_dpp v48, v48 row_shr:1 row_mask:0xf bank_mask:0xf bound_ctrl:1
	v_mov_b32_dpp v49, v49 row_shr:1 row_mask:0xf bank_mask:0xf bound_ctrl:1
	v_pk_fma_f32 v[38:39], v[38:39], s[6:7], v[48:49] op_sel_hi:[1,0,1]
	s_nop 1
	v_add_f32_dpp v38, v38, v38 row_shr:2 row_mask:0xf bank_mask:0xf bound_ctrl:1
	v_add_f32_dpp v39, v39, v39 row_shr:2 row_mask:0xf bank_mask:0xf bound_ctrl:1
	s_nop 1
	v_add_f32_dpp v38, v38, v38 row_shr:4 row_mask:0xf bank_mask:0xf bound_ctrl:1
	v_add_f32_dpp v39, v39, v39 row_shr:4 row_mask:0xf bank_mask:0xf bound_ctrl:1
	s_nop 1
	v_add_f32_dpp v38, v38, v38 row_shr:8 row_mask:0xf bank_mask:0xf bound_ctrl:1
	v_add_f32_dpp v39, v39, v39 row_shr:8 row_mask:0xf bank_mask:0xf bound_ctrl:1
	v_pk_mul_f32 v[48:49], v[36:37], s[6:7] op_sel_hi:[1,0]
	v_cvt_pk_f16_f32 v33, v38, v39
	s_nop 0
	v_mov_b32_dpp v48, v48 row_shr:1 row_mask:0xf bank_mask:0xf bound_ctrl:1
	v_mov_b32_dpp v49, v49 row_shr:1 row_mask:0xf bank_mask:0xf bound_ctrl:1
	v_pk_fma_f32 v[36:37], v[36:37], s[6:7], v[48:49] op_sel_hi:[1,0,1]
	s_nop 1
	v_add_f32_dpp v36, v36, v36 row_shr:2 row_mask:0xf bank_mask:0xf bound_ctrl:1
	v_add_f32_dpp v37, v37, v37 row_shr:2 row_mask:0xf bank_mask:0xf bound_ctrl:1
	s_nop 1
	v_add_f32_dpp v36, v36, v36 row_shr:4 row_mask:0xf bank_mask:0xf bound_ctrl:1
	v_add_f32_dpp v37, v37, v37 row_shr:4 row_mask:0xf bank_mask:0xf bound_ctrl:1
	s_nop 1
	v_add_f32_dpp v36, v36, v36 row_shr:8 row_mask:0xf bank_mask:0xf bound_ctrl:1
	v_add_f32_dpp v37, v37, v37 row_shr:8 row_mask:0xf bank_mask:0xf bound_ctrl:1
	s_nop 0
	v_cvt_pk_f16_f32 v35, v36, v37

.LBB0_774:
	v_pk_mul_f32 v[24:25], v[34:35], s[6:7] op_sel_hi:[1,0]
	s_nop 1
	v_mov_b32_dpp v24, v24 row_shr:1 row_mask:0xf bank_mask:0xf bound_ctrl:1
	v_mov_b32_dpp v25, v25 row_shr:1 row_mask:0xf bank_mask:0xf bound_ctrl:1
	v_pk_fma_f32 v[24:25], v[34:35], s[6:7], v[24:25] op_sel_hi:[1,0,1]
	s_nop 1
	v_add_f32_dpp v24, v24, v24 row_shr:2 row_mask:0xf bank_mask:0xf bound_ctrl:1
	v_add_f32_dpp v25, v25, v25 row_shr:2 row_mask:0xf bank_mask:0xf bound_ctrl:1
	s_nop 1
	v_add_f32_dpp v24, v24, v24 row_shr:4 row_mask:0xf bank_mask:0xf bound_ctrl:1
	v_add_f32_dpp v25, v25, v25 row_shr:4 row_mask:0xf bank_mask:0xf bound_ctrl:1
	s_nop 1
	v_add_f32_dpp v24, v24, v24 row_shr:8 row_mask:0xf bank_mask:0xf bound_ctrl:1
	v_add_f32_dpp v25, v25, v25 row_shr:8 row_mask:0xf bank_mask:0xf bound_ctrl:1
	v_pk_mul_f32 v[26:27], v[32:33], s[6:7] op_sel_hi:[1,0]
	v_cvt_pk_f16_f32 v24, v24, v25
	s_nop 0
	v_mov_b32_dpp v26, v26 row_shr:1 row_mask:0xf bank_mask:0xf bound_ctrl:1
	v_mov_b32_dpp v27, v27 row_shr:1 row_mask:0xf bank_mask:0xf bound_ctrl:1
	v_pk_fma_f32 v[26:27], v[32:33], s[6:7], v[26:27] op_sel_hi:[1,0,1]
	s_nop 1
	v_add_f32_dpp v26, v26, v26 row_shr:2 row_mask:0xf bank_mask:0xf bound_ctrl:1
	v_add_f32_dpp v27, v27, v27 row_shr:2 row_mask:0xf bank_mask:0xf bound_ctrl:1
	s_nop 1
	v_add_f32_dpp v26, v26, v26 row_shr:4 row_mask:0xf bank_mask:0xf bound_ctrl:1
	v_add_f32_dpp v27, v27, v27 row_shr:4 row_mask:0xf bank_mask:0xf bound_ctrl:1
	s_nop 1
	v_add_f32_dpp v26, v26, v26 row_shr:8 row_mask:0xf bank_mask:0xf bound_ctrl:1
	v_add_f32_dpp v27, v27, v27 row_shr:8 row_mask:0xf bank_mask:0xf bound_ctrl:1
	v_pk_mul_f32 v[32:33], v[30:31], s[6:7] op_sel_hi:[1,0]
	v_cvt_pk_f16_f32 v26, v26, v27
	s_nop 0
	v_mov_b32_dpp v32, v32 row_shr:1 row_mask:0xf bank_mask:0xf bound_ctrl:1
	v_mov_b32_dpp v33, v33 row_shr:1 row_mask:0xf bank_mask:0xf bound_ctrl:1
	v_pk_fma_f32 v[30:31], v[30:31], s[6:7], v[32:33] op_sel_hi:[1,0,1]
	s_nop 1
	v_add_f32_dpp v30, v30, v30 row_shr:2 row_mask:0xf bank_mask:0xf bound_ctrl:1
	v_add_f32_dpp v31, v31, v31 row_shr:2 row_mask:0xf bank_mask:0xf bound_ctrl:1
	s_nop 1
	v_add_f32_dpp v30, v30, v30 row_shr:4 row_mask:0xf bank_mask:0xf bound_ctrl:1
	v_add_f32_dpp v31, v31, v31 row_shr:4 row_mask:0xf bank_mask:0xf bound_ctrl:1
	s_nop 1
	v_add_f32_dpp v30, v30, v30 row_shr:8 row_mask:0xf bank_mask:0xf bound_ctrl:1
	v_add_f32_dpp v31, v31, v31 row_shr:8 row_mask:0xf bank_mask:0xf bound_ctrl:1
	v_pk_mul_f32 v[32:33], v[28:29], s[6:7] op_sel_hi:[1,0]
	v_cvt_pk_f16_f32 v25, v30, v31
	s_nop 0
	v_mov_b32_dpp v32, v32 row_shr:1 row_mask:0xf bank_mask:0xf bound_ctrl:1
	v_mov_b32_dpp v33, v33 row_shr:1 row_mask:0xf bank_mask:0xf bound_ctrl:1
	v_pk_fma_f32 v[28:29], v[28:29], s[6:7], v[32:33] op_sel_hi:[1,0,1]
	s_nop 1
	v_add_f32_dpp v28, v28, v28 row_shr:2 row_mask:0xf bank_mask:0xf bound_ctrl:1
	v_add_f32_dpp v29, v29, v29 row_shr:2 row_mask:0xf bank_mask:0xf bound_ctrl:1
	s_nop 1
	v_add_f32_dpp v28, v28, v28 row_shr:4 row_mask:0xf bank_mask:0xf bound_ctrl:1
	v_add_f32_dpp v29, v29, v29 row_shr:4 row_mask:0xf bank_mask:0xf bound_ctrl:1
	s_nop 1
	v_add_f32_dpp v28, v28, v28 row_shr:8 row_mask:0xf bank_mask:0xf bound_ctrl:1
	v_add_f32_dpp v29, v29, v29 row_shr:8 row_mask:0xf bank_mask:0xf bound_ctrl:1
	s_nop 0
	v_cvt_pk_f16_f32 v27, v28, v29

.LBB0_778:
	v_pk_mul_f32 v[16:17], v[26:27], s[6:7] op_sel_hi:[1,0]
	s_nop 1
	v_mov_b32_dpp v16, v16 row_shr:1 row_mask:0xf bank_mask:0xf bound_ctrl:1
	v_mov_b32_dpp v17, v17 row_shr:1 row_mask:0xf bank_mask:0xf bound_ctrl:1
	v_pk_fma_f32 v[16:17], v[26:27], s[6:7], v[16:17] op_sel_hi:[1,0,1]
	s_nop 1
	v_add_f32_dpp v16, v16, v16 row_shr:2 row_mask:0xf bank_mask:0xf bound_ctrl:1
	v_add_f32_dpp v17, v17, v17 row_shr:2 row_mask:0xf bank_mask:0xf bound_ctrl:1
	s_nop 1
	v_add_f32_dpp v16, v16, v16 row_shr:4 row_mask:0xf bank_mask:0xf bound_ctrl:1
	v_add_f32_dpp v17, v17, v17 row_shr:4 row_mask:0xf bank_mask:0xf bound_ctrl:1
	s_nop 1
	v_add_f32_dpp v16, v16, v16 row_shr:8 row_mask:0xf bank_mask:0xf bound_ctrl:1
	v_add_f32_dpp v17, v17, v17 row_shr:8 row_mask:0xf bank_mask:0xf bound_ctrl:1
	v_pk_mul_f32 v[18:19], v[24:25], s[6:7] op_sel_hi:[1,0]
	v_cvt_pk_f16_f32 v16, v16, v17
	s_nop 0
	v_mov_b32_dpp v18, v18 row_shr:1 row_mask:0xf bank_mask:0xf bound_ctrl:1
	v_mov_b32_dpp v19, v19 row_shr:1 row_mask:0xf bank_mask:0xf bound_ctrl:1
	v_pk_fma_f32 v[18:19], v[24:25], s[6:7], v[18:19] op_sel_hi:[1,0,1]
	s_nop 1
	v_add_f32_dpp v18, v18, v18 row_shr:2 row_mask:0xf bank_mask:0xf bound_ctrl:1
	v_add_f32_dpp v19, v19, v19 row_shr:2 row_mask:0xf bank_mask:0xf bound_ctrl:1
	s_nop 1
	v_add_f32_dpp v18, v18, v18 row_shr:4 row_mask:0xf bank_mask:0xf bound_ctrl:1
	v_add_f32_dpp v19, v19, v19 row_shr:4 row_mask:0xf bank_mask:0xf bound_ctrl:1
	s_nop 1
	v_add_f32_dpp v18, v18, v18 row_shr:8 row_mask:0xf bank_mask:0xf bound_ctrl:1
	v_add_f32_dpp v19, v19, v19 row_shr:8 row_mask:0xf bank_mask:0xf bound_ctrl:1
	v_pk_mul_f32 v[24:25], v[22:23], s[6:7] op_sel_hi:[1,0]
	v_cvt_pk_f16_f32 v18, v18, v19
	s_nop 0
	v_mov_b32_dpp v24, v24 row_shr:1 row_mask:0xf bank_mask:0xf bound_ctrl:1
	v_mov_b32_dpp v25, v25 row_shr:1 row_mask:0xf bank_mask:0xf bound_ctrl:1
	v_pk_fma_f32 v[22:23], v[22:23], s[6:7], v[24:25] op_sel_hi:[1,0,1]
	s_nop 1
	v_add_f32_dpp v22, v22, v22 row_shr:2 row_mask:0xf bank_mask:0xf bound_ctrl:1
	v_add_f32_dpp v23, v23, v23 row_shr:2 row_mask:0xf bank_mask:0xf bound_ctrl:1
	s_nop 1
	v_add_f32_dpp v22, v22, v22 row_shr:4 row_mask:0xf bank_mask:0xf bound_ctrl:1
	v_add_f32_dpp v23, v23, v23 row_shr:4 row_mask:0xf bank_mask:0xf bound_ctrl:1
	s_nop 1
	v_add_f32_dpp v22, v22, v22 row_shr:8 row_mask:0xf bank_mask:0xf bound_ctrl:1
	v_add_f32_dpp v23, v23, v23 row_shr:8 row_mask:0xf bank_mask:0xf bound_ctrl:1
	v_pk_mul_f32 v[24:25], v[20:21], s[6:7] op_sel_hi:[1,0]
	v_cvt_pk_f16_f32 v17, v22, v23
	s_nop 0
	v_mov_b32_dpp v24, v24 row_shr:1 row_mask:0xf bank_mask:0xf bound_ctrl:1
	v_mov_b32_dpp v25, v25 row_shr:1 row_mask:0xf bank_mask:0xf bound_ctrl:1
	v_pk_fma_f32 v[20:21], v[20:21], s[6:7], v[24:25] op_sel_hi:[1,0,1]
	s_nop 1
	v_add_f32_dpp v20, v20, v20 row_shr:2 row_mask:0xf bank_mask:0xf bound_ctrl:1
	v_add_f32_dpp v21, v21, v21 row_shr:2 row_mask:0xf bank_mask:0xf bound_ctrl:1
	s_nop 1
	v_add_f32_dpp v20, v20, v20 row_shr:4 row_mask:0xf bank_mask:0xf bound_ctrl:1
	v_add_f32_dpp v21, v21, v21 row_shr:4 row_mask:0xf bank_mask:0xf bound_ctrl:1
	s_nop 1
	v_add_f32_dpp v20, v20, v20 row_shr:8 row_mask:0xf bank_mask:0xf bound_ctrl:1
	v_add_f32_dpp v21, v21, v21 row_shr:8 row_mask:0xf bank_mask:0xf bound_ctrl:1
	s_nop 0
	v_cvt_pk_f16_f32 v19, v20, v21

.LBB0_782:
	v_pk_mul_f32 v[8:9], v[18:19], s[6:7] op_sel_hi:[1,0]
	s_nop 1
	v_mov_b32_dpp v8, v8 row_shr:1 row_mask:0xf bank_mask:0xf bound_ctrl:1
	v_mov_b32_dpp v9, v9 row_shr:1 row_mask:0xf bank_mask:0xf bound_ctrl:1
	v_pk_fma_f32 v[8:9], v[18:19], s[6:7], v[8:9] op_sel_hi:[1,0,1]
	s_nop 1
	v_add_f32_dpp v8, v8, v8 row_shr:2 row_mask:0xf bank_mask:0xf bound_ctrl:1
	v_add_f32_dpp v9, v9, v9 row_shr:2 row_mask:0xf bank_mask:0xf bound_ctrl:1
	s_nop 1
	v_add_f32_dpp v8, v8, v8 row_shr:4 row_mask:0xf bank_mask:0xf bound_ctrl:1
	v_add_f32_dpp v9, v9, v9 row_shr:4 row_mask:0xf bank_mask:0xf bound_ctrl:1
	s_nop 1
	v_add_f32_dpp v8, v8, v8 row_shr:8 row_mask:0xf bank_mask:0xf bound_ctrl:1
	v_add_f32_dpp v9, v9, v9 row_shr:8 row_mask:0xf bank_mask:0xf bound_ctrl:1
	v_pk_mul_f32 v[10:11], v[16:17], s[6:7] op_sel_hi:[1,0]
	v_cvt_pk_f16_f32 v8, v8, v9
	s_nop 0
	v_mov_b32_dpp v10, v10 row_shr:1 row_mask:0xf bank_mask:0xf bound_ctrl:1
	v_mov_b32_dpp v11, v11 row_shr:1 row_mask:0xf bank_mask:0xf bound_ctrl:1
	v_pk_fma_f32 v[10:11], v[16:17], s[6:7], v[10:11] op_sel_hi:[1,0,1]
	s_nop 1
	v_add_f32_dpp v10, v10, v10 row_shr:2 row_mask:0xf bank_mask:0xf bound_ctrl:1
	v_add_f32_dpp v11, v11, v11 row_shr:2 row_mask:0xf bank_mask:0xf bound_ctrl:1
	s_nop 1
	v_add_f32_dpp v10, v10, v10 row_shr:4 row_mask:0xf bank_mask:0xf bound_ctrl:1
	v_add_f32_dpp v11, v11, v11 row_shr:4 row_mask:0xf bank_mask:0xf bound_ctrl:1
	s_nop 1
	v_add_f32_dpp v10, v10, v10 row_shr:8 row_mask:0xf bank_mask:0xf bound_ctrl:1
	v_add_f32_dpp v11, v11, v11 row_shr:8 row_mask:0xf bank_mask:0xf bound_ctrl:1
	v_pk_mul_f32 v[16:17], v[14:15], s[6:7] op_sel_hi:[1,0]
	v_cvt_pk_f16_f32 v10, v10, v11
	s_nop 0
	v_mov_b32_dpp v16, v16 row_shr:1 row_mask:0xf bank_mask:0xf bound_ctrl:1
	v_mov_b32_dpp v17, v17 row_shr:1 row_mask:0xf bank_mask:0xf bound_ctrl:1
	v_pk_fma_f32 v[14:15], v[14:15], s[6:7], v[16:17] op_sel_hi:[1,0,1]
	s_nop 1
	v_add_f32_dpp v14, v14, v14 row_shr:2 row_mask:0xf bank_mask:0xf bound_ctrl:1
	v_add_f32_dpp v15, v15, v15 row_shr:2 row_mask:0xf bank_mask:0xf bound_ctrl:1
	s_nop 1
	v_add_f32_dpp v14, v14, v14 row_shr:4 row_mask:0xf bank_mask:0xf bound_ctrl:1
	v_add_f32_dpp v15, v15, v15 row_shr:4 row_mask:0xf bank_mask:0xf bound_ctrl:1
	s_nop 1
	v_add_f32_dpp v14, v14, v14 row_shr:8 row_mask:0xf bank_mask:0xf bound_ctrl:1
	v_add_f32_dpp v15, v15, v15 row_shr:8 row_mask:0xf bank_mask:0xf bound_ctrl:1
	v_pk_mul_f32 v[16:17], v[12:13], s[6:7] op_sel_hi:[1,0]
	v_cvt_pk_f16_f32 v9, v14, v15
	s_nop 0
	v_mov_b32_dpp v16, v16 row_shr:1 row_mask:0xf bank_mask:0xf bound_ctrl:1
	v_mov_b32_dpp v17, v17 row_shr:1 row_mask:0xf bank_mask:0xf bound_ctrl:1
	v_pk_fma_f32 v[12:13], v[12:13], s[6:7], v[16:17] op_sel_hi:[1,0,1]
	s_nop 1
	v_add_f32_dpp v12, v12, v12 row_shr:2 row_mask:0xf bank_mask:0xf bound_ctrl:1
	v_add_f32_dpp v13, v13, v13 row_shr:2 row_mask:0xf bank_mask:0xf bound_ctrl:1
	s_nop 1
	v_add_f32_dpp v12, v12, v12 row_shr:4 row_mask:0xf bank_mask:0xf bound_ctrl:1
	v_add_f32_dpp v13, v13, v13 row_shr:4 row_mask:0xf bank_mask:0xf bound_ctrl:1
	s_nop 1
	v_add_f32_dpp v12, v12, v12 row_shr:8 row_mask:0xf bank_mask:0xf bound_ctrl:1
	v_add_f32_dpp v13, v13, v13 row_shr:8 row_mask:0xf bank_mask:0xf bound_ctrl:1
	s_nop 0
	v_cvt_pk_f16_f32 v11, v12, v13

.LBB0_816:
	v_pk_mul_f32 v[0:1], v[10:11], s[6:7] op_sel_hi:[1,0]
	s_nop 1
	v_mov_b32_dpp v0, v0 row_shr:1 row_mask:0xf bank_mask:0xf bound_ctrl:1
	v_mov_b32_dpp v1, v1 row_shr:1 row_mask:0xf bank_mask:0xf bound_ctrl:1
	v_pk_fma_f32 v[0:1], v[10:11], s[6:7], v[0:1] op_sel_hi:[1,0,1]
	s_nop 1
	v_add_f32_dpp v0, v0, v0 row_shr:2 row_mask:0xf bank_mask:0xf bound_ctrl:1
	v_add_f32_dpp v1, v1, v1 row_shr:2 row_mask:0xf bank_mask:0xf bound_ctrl:1
	s_nop 1
	v_add_f32_dpp v0, v0, v0 row_shr:4 row_mask:0xf bank_mask:0xf bound_ctrl:1
	v_add_f32_dpp v1, v1, v1 row_shr:4 row_mask:0xf bank_mask:0xf bound_ctrl:1
	s_nop 1
	v_add_f32_dpp v0, v0, v0 row_shr:8 row_mask:0xf bank_mask:0xf bound_ctrl:1
	v_add_f32_dpp v1, v1, v1 row_shr:8 row_mask:0xf bank_mask:0xf bound_ctrl:1
	v_pk_mul_f32 v[2:3], v[8:9], s[6:7] op_sel_hi:[1,0]
	v_cvt_pk_f16_f32 v0, v0, v1
	s_nop 0
	v_mov_b32_dpp v2, v2 row_shr:1 row_mask:0xf bank_mask:0xf bound_ctrl:1
	v_mov_b32_dpp v3, v3 row_shr:1 row_mask:0xf bank_mask:0xf bound_ctrl:1
	v_pk_fma_f32 v[2:3], v[8:9], s[6:7], v[2:3] op_sel_hi:[1,0,1]
	s_nop 1
	v_add_f32_dpp v2, v2, v2 row_shr:2 row_mask:0xf bank_mask:0xf bound_ctrl:1
	v_add_f32_dpp v3, v3, v3 row_shr:2 row_mask:0xf bank_mask:0xf bound_ctrl:1
	s_nop 1
	v_add_f32_dpp v2, v2, v2 row_shr:4 row_mask:0xf bank_mask:0xf bound_ctrl:1
	v_add_f32_dpp v3, v3, v3 row_shr:4 row_mask:0xf bank_mask:0xf bound_ctrl:1
	s_nop 1
	v_add_f32_dpp v2, v2, v2 row_shr:8 row_mask:0xf bank_mask:0xf bound_ctrl:1
	v_add_f32_dpp v3, v3, v3 row_shr:8 row_mask:0xf bank_mask:0xf bound_ctrl:1
	v_pk_mul_f32 v[8:9], v[6:7], s[6:7] op_sel_hi:[1,0]
	v_cvt_pk_f16_f32 v2, v2, v3
	s_nop 0
	v_mov_b32_dpp v8, v8 row_shr:1 row_mask:0xf bank_mask:0xf bound_ctrl:1
	v_mov_b32_dpp v9, v9 row_shr:1 row_mask:0xf bank_mask:0xf bound_ctrl:1
	v_pk_fma_f32 v[6:7], v[6:7], s[6:7], v[8:9] op_sel_hi:[1,0,1]
	s_nop 1
	v_add_f32_dpp v6, v6, v6 row_shr:2 row_mask:0xf bank_mask:0xf bound_ctrl:1
	v_add_f32_dpp v7, v7, v7 row_shr:2 row_mask:0xf bank_mask:0xf bound_ctrl:1
	s_nop 1
	v_add_f32_dpp v6, v6, v6 row_shr:4 row_mask:0xf bank_mask:0xf bound_ctrl:1
	v_add_f32_dpp v7, v7, v7 row_shr:4 row_mask:0xf bank_mask:0xf bound_ctrl:1
	s_nop 1
	v_add_f32_dpp v6, v6, v6 row_shr:8 row_mask:0xf bank_mask:0xf bound_ctrl:1
	v_add_f32_dpp v7, v7, v7 row_shr:8 row_mask:0xf bank_mask:0xf bound_ctrl:1
	v_pk_mul_f32 v[8:9], v[4:5], s[6:7] op_sel_hi:[1,0]
	v_cvt_pk_f16_f32 v1, v6, v7
	s_nop 0
	v_mov_b32_dpp v8, v8 row_shr:1 row_mask:0xf bank_mask:0xf bound_ctrl:1
	v_mov_b32_dpp v9, v9 row_shr:1 row_mask:0xf bank_mask:0xf bound_ctrl:1
	v_pk_fma_f32 v[4:5], v[4:5], s[6:7], v[8:9] op_sel_hi:[1,0,1]
	s_nop 1
	v_add_f32_dpp v4, v4, v4 row_shr:2 row_mask:0xf bank_mask:0xf bound_ctrl:1
	v_add_f32_dpp v5, v5, v5 row_shr:2 row_mask:0xf bank_mask:0xf bound_ctrl:1
	s_nop 1
	v_add_f32_dpp v4, v4, v4 row_shr:4 row_mask:0xf bank_mask:0xf bound_ctrl:1
	v_add_f32_dpp v5, v5, v5 row_shr:4 row_mask:0xf bank_mask:0xf bound_ctrl:1
	s_nop 1
	v_add_f32_dpp v4, v4, v4 row_shr:8 row_mask:0xf bank_mask:0xf bound_ctrl:1
	v_add_f32_dpp v5, v5, v5 row_shr:8 row_mask:0xf bank_mask:0xf bound_ctrl:1
	s_nop 0
	v_cvt_pk_f16_f32 v3, v4, v5
	s_branch .LBB0_707
